# row reductions in the out-projection epilogue and retention statistics: lane^16/lane^32 exchanges via v_permlane16/32_swap instead of LDS ds_swizzle/ds_bpermute round trips
# speedup vs baseline: 1.0065x; 1.0065x over previous
; template <int VAR  >
; __device__ __forceinline__ void ret_core_mfma(const bf16* P, const bf16* VT, const float* decay_logit  , bf16* YF, bf16* YB, float* PT, LAS unsigned char* lds, const int tid, const int bid, const int G) {
;     ...
;             for (int ks = 0; ks < 8; ++ks) {
;                 if (ks < 4) { if (c == 0) RC_WAITV(6); else RC_WAITV(14); } else if (ks == 4) RC_WAITV(6); else if (ks == 5) RC_WAITV(5); else if (ks == 6) RC_WAITV(4); else RC_WAITV(3);
;                 RC_BAR();
;                 { const int s4 = RC_PREV(slot);
;                   if (ks + 4 < 12) RC_ISSUE(ks + 4, tok0, s4); else RC_ISSUE(ks + 4 - 12, tokn, s4); }
;                 bf16x8v At[4], Bk[2], Bs[2];
;                 const LAS unsigned char* sq = lds + RC_RG + slot * 16384;
; #pragma unroll
;                 for (int m = 0; m < 4; ++m) At[m] = *(const LAS bf16x8v*)(sq + aoff + m * 1024);
; #pragma unroll
;                 for (int n = 0; n < 2; ++n) { Bk[n] = *(const LAS bf16x8v*)(sq + 8192 + boff + n * 1024); Bs[n] = *(const LAS bf16x8v*)(lds + RC_ST + ks * 8192 + boff + n * 1024); }
; #pragma unroll
;                 for (int m = 0; m < 4; ++m)
; #pragma unroll
;                     for (int n = 0; n < 2; ++n) { accA[m][n] = RC_MFMA(Bk[n], At[m], accA[m][n]); accY[m][n] = RC_MFMA(Bs[n], At[m], accY[m][n]); }
;                 { const unsigned kb = (unsigned)(size_t)(sq + 8192);
;                   const unsigned a0 = kb + trA, a1 = kb + trB, b0 = kb + (trA ^ 32u), b1 = kb + (trB ^ 32u);
;                   v2u l0, h0, l1, h1, l2, h2, l3, h3, p0, q0, p1, q1, p2, q2, p3, q3;
;                   asm volatile("ds_read_b64_tr_b16 %0, %16\n\tds_read_b64_tr_b16 %1, %17\n\tds_read_b64_tr_b16 %8, %18\n\tds_read_b64_tr_b16 %9, %19\n\t"
;                                "ds_read_b64_tr_b16 %2, %16 offset:2048\n\tds_read_b64_tr_b16 %3, %17 offset:2048\n\tds_read_b64_tr_b16 %10, %18 offset:2048\n\tds_read_b64_tr_b16 %11, %19 offset:2048\n\t"
;                                "ds_read_b64_tr_b16 %4, %16 offset:4096\n\tds_read_b64_tr_b16 %5, %17 offset:4096\n\tds_read_b64_tr_b16 %12, %18 offset:4096\n\tds_read_b64_tr_b16 %13, %19 offset:4096\n\t"
;                                "ds_read_b64_tr_b16 %6, %16 offset:6144\n\tds_read_b64_tr_b16 %7, %17 offset:6144\n\tds_read_b64_tr_b16 %14, %18 offset:6144\n\tds_read_b64_tr_b16 %15, %19 offset:6144\n\ts_waitcnt lgkmcnt(0)"
.LBB0_55:
	s_add_i32 s0, s40, 1
	s_cmp_lg_u32 s40, 4
	s_cselect_b32 s0, s0, 0
	s_lshl_b32 s60, s38, 7
	s_add_i32 s6, s33, 1
	s_cmp_eq_u32 s33, 15
	s_cselect_b32 s1, 0, s39
	s_cselect_b32 s7, 15, s6
	s_and_b64 s[40:41], s[4:5], exec
	s_cselect_b32 s7, s7, s1
	s_lshl_b32 s1, s0, 14
	s_lshl_b32 s40, s38, 8
	s_add_i32 s33, s1, 0xffffc000
	s_cmp_lg_u32 s0, 0
	s_cselect_b32 s33, s33, 0x10000
	s_mov_b32 s41, s61
	s_add_i32 s33, s33, 0
	v_lshl_add_u64 v[148:149], v[220:221], 0, s[40:41]
	s_mov_b64 s[40:41], 0x1c0
	s_add_i32 s33, s33, s44
	s_barrier
	v_lshl_add_u64 v[150:151], v[232:233], 0, s[40:41]
	s_add_i32 m0, s33, 0x10000
	s_mov_b64 s[40:41], 0x9c0
	global_load_lds_dwordx4 v[150:151], off
	v_lshl_add_u64 v[150:151], v[232:233], 0, s[40:41]
	s_add_i32 m0, s33, 0x12000
	s_add_i32 s1, s86, s1
	global_load_lds_dwordx4 v[150:151], off
	v_add_u32_e32 v170, s1, v242
	v_add_u32_e32 v178, s1, v243
	ds_read_b128 v[150:153], v236 offset:25600
	ds_read_b128 v[154:157], v236 offset:24576
	ds_read_b128 v[158:161], v170
	ds_read_b128 v[162:165], v170 offset:1024
	ds_read_b128 v[166:169], v170 offset:2048
	ds_read_b128 v[170:173], v170 offset:3072
	ds_read_b128 v[174:177], v178 offset:8192
	ds_read_b128 v[178:181], v178 offset:9216
	v_mov_b32_e32 v217, v216
	v_pk_mul_f32 v[26:27], v[216:217], v[26:27]
	v_pk_mul_f32 v[24:25], v[224:225], v[24:25]
	v_pk_mul_f32 v[22:23], v[216:217], v[22:23]
	v_pk_mul_f32 v[20:21], v[224:225], v[20:21]
	s_add_i32 s33, s1, 0x2000
	s_waitcnt lgkmcnt(0)
	v_mfma_f32_16x16x32_bf16 v[96:99], v[174:177], v[158:161], v[96:99]
	v_add_u32_e32 v182, s33, v234
	v_add_u32_e32 v183, s33, v231
	v_add_u32_e32 v184, s33, v227
	v_mfma_f32_16x16x32_bf16 v[100:103], v[154:157], v[158:161], v[100:103]
	v_add_u32_e32 v185, s33, v229
	s_add_i32 s1, s0, 1
	s_cmp_lg_u32 s0, 4
	v_mfma_f32_16x16x32_bf16 v[104:107], v[178:181], v[158:161], v[104:107]
	s_cselect_b32 s0, s1, 0
	s_lshl_b32 s1, s0, 14
	s_add_i32 s33, s1, 0xffffc000
	v_mfma_f32_16x16x32_bf16 v[108:111], v[150:153], v[158:161], v[108:111]
	s_cmp_lg_u32 s0, 0
	s_cselect_b32 s33, s33, 0x10000
	s_add_i32 s33, s33, 0
	v_mfma_f32_16x16x32_bf16 v[112:115], v[174:177], v[162:165], v[112:115]
	s_add_i32 s33, s33, s44
	s_add_i32 m0, s33, 0x10000
	s_add_i32 s1, s86, s1
	v_mfma_f32_16x16x32_bf16 v[116:119], v[154:157], v[162:165], v[116:119]
	v_mul_f32_e64 v30, v216, v30
	v_mul_f32_e64 v31, v217, v31
	v_pk_mul_f32 v[28:29], v[224:225], v[28:29]
	s_add_i32 s33, s1, 0x2000
	v_mfma_f32_16x16x32_bf16 v[120:123], v[178:181], v[162:165], v[120:123]
	v_mul_f32_e64 v34, v216, v34
	v_mul_f32_e64 v35, v217, v35
	v_pk_mul_f32 v[32:33], v[224:225], v[32:33]
	v_pk_mul_f32 v[46:47], v[216:217], v[46:47]
	v_mfma_f32_16x16x32_bf16 v[124:127], v[150:153], v[162:165], v[124:127]
	v_mul_f32_e64 v44, v224, v44
	v_mul_f32_e64 v45, v225, v45
	v_pk_mul_f32 v[50:51], v[216:217], v[50:51]
	v_pk_mul_f32 v[48:49], v[224:225], v[48:49]
	v_mfma_f32_16x16x32_bf16 v[128:131], v[174:177], v[166:169], v[128:131]
	v_mul_f32_e64 v58, v216, v58
	v_mul_f32_e64 v59, v217, v59
	v_pk_mul_f32 v[56:57], v[224:225], v[56:57]
	v_pk_mul_f32 v[54:55], v[216:217], v[54:55]
	v_mfma_f32_16x16x32_bf16 v[132:135], v[154:157], v[166:169], v[132:135]
	v_mul_f32_e64 v52, v224, v52
	v_mul_f32_e64 v53, v225, v53
	v_pk_mul_f32 v[62:63], v[216:217], v[62:63]
	v_pk_mul_f32 v[60:61], v[224:225], v[60:61]
	v_mfma_f32_16x16x32_bf16 v[136:139], v[178:181], v[166:169], v[136:139]
	v_mul_f32_e64 v66, v216, v66
	v_mul_f32_e64 v67, v217, v67
	v_pk_mul_f32 v[64:65], v[224:225], v[64:65]
	v_and_b32_e32 v2, 15, v230
	v_mfma_f32_16x16x32_bf16 v[140:143], v[150:153], v[166:169], v[140:143]
	v_mfma_f32_16x16x32_bf16 v[144:147], v[174:177], v[170:173], v[144:147]
	v_mfma_f32_16x16x32_bf16 v[88:91], v[154:157], v[170:173], v[88:91]
	v_mfma_f32_16x16x32_bf16 v[84:87], v[178:181], v[170:173], v[84:87]
	v_mfma_f32_16x16x32_bf16 v[92:95], v[150:153], v[170:173], v[92:95]
	ds_read_b64_tr_b16 v[178:179], v182
	ds_read_b64_tr_b16 v[180:181], v183
	ds_read_b64_tr_b16 v[174:175], v184
	ds_read_b64_tr_b16 v[176:177], v185
	ds_read_b64_tr_b16 v[170:171], v182 offset:2048
	ds_read_b64_tr_b16 v[172:173], v183 offset:2048
	ds_read_b64_tr_b16 v[166:167], v184 offset:2048
	ds_read_b64_tr_b16 v[168:169], v185 offset:2048
	ds_read_b64_tr_b16 v[162:163], v182 offset:4096
	ds_read_b64_tr_b16 v[164:165], v183 offset:4096
	ds_read_b64_tr_b16 v[158:159], v184 offset:4096
	ds_read_b64_tr_b16 v[160:161], v185 offset:4096
	ds_read_b64_tr_b16 v[154:155], v182 offset:6144
	ds_read_b64_tr_b16 v[156:157], v183 offset:6144
	ds_read_b64_tr_b16 v[150:151], v184 offset:6144
	ds_read_b64_tr_b16 v[152:153], v185 offset:6144
	s_waitcnt lgkmcnt(0)
	s_waitcnt vmcnt(6)
	s_barrier
; template <int VAR  >
; __device__ __forceinline__ void ret_core_mfma(const bf16* P, const bf16* VT, const float* decay_logit  , bf16* YF, bf16* YB, float* PT, LAS unsigned char* lds, const int tid, const int bid, const int G) {
;     ...
;             for (int ks = 0; ks < 8; ++ks) {
;                 if (ks < 4) { if (c == 0) RC_WAITV(6); else RC_WAITV(14); } else if (ks == 4) RC_WAITV(6); else if (ks == 5) RC_WAITV(5); else if (ks == 6) RC_WAITV(4); else RC_WAITV(3);
;                 RC_BAR();
;                 { const int s4 = RC_PREV(slot);
;                   if (ks + 4 < 12) RC_ISSUE(ks + 4, tok0, s4); else RC_ISSUE(ks + 4 - 12, tokn, s4); }
;                 bf16x8v At[4], Bk[2], Bs[2];
;                 const LAS unsigned char* sq = lds + RC_RG + slot * 16384;
; #pragma unroll
;                 for (int m = 0; m < 4; ++m) At[m] = *(const LAS bf16x8v*)(sq + aoff + m * 1024);
; #pragma unroll
;                 for (int n = 0; n < 2; ++n) { Bk[n] = *(const LAS bf16x8v*)(sq + 8192 + boff + n * 1024); Bs[n] = *(const LAS bf16x8v*)(lds + RC_ST + ks * 8192 + boff + n * 1024); }
; #pragma unroll
;                 for (int m = 0; m < 4; ++m)
; #pragma unroll
;                     for (int n = 0; n < 2; ++n) { accA[m][n] = RC_MFMA(Bk[n], At[m], accA[m][n]); accY[m][n] = RC_MFMA(Bs[n], At[m], accY[m][n]); }
;                 { const unsigned kb = (unsigned)(size_t)(sq + 8192);
;                   const unsigned a0 = kb + trA, a1 = kb + trB, b0 = kb + (trA ^ 32u), b1 = kb + (trB ^ 32u);
;                   v2u l0, h0, l1, h1, l2, h2, l3, h3, p0, q0, p1, q1, p2, q2, p3, q3;
;                   asm volatile("ds_read_b64_tr_b16 %0, %16\n\tds_read_b64_tr_b16 %1, %17\n\tds_read_b64_tr_b16 %8, %18\n\tds_read_b64_tr_b16 %9, %19\n\t"
;                                "ds_read_b64_tr_b16 %2, %16 offset:2048\n\tds_read_b64_tr_b16 %3, %17 offset:2048\n\tds_read_b64_tr_b16 %10, %18 offset:2048\n\tds_read_b64_tr_b16 %11, %19 offset:2048\n\t"
;                                "ds_read_b64_tr_b16 %4, %16 offset:4096\n\tds_read_b64_tr_b16 %5, %17 offset:4096\n\tds_read_b64_tr_b16 %12, %18 offset:4096\n\tds_read_b64_tr_b16 %13, %19 offset:4096\n\t"
;                                "ds_read_b64_tr_b16 %6, %16 offset:6144\n\tds_read_b64_tr_b16 %7, %17 offset:6144\n\tds_read_b64_tr_b16 %14, %18 offset:6144\n\tds_read_b64_tr_b16 %15, %19 offset:6144\n\ts_waitcnt lgkmcnt(0)"
	v_mfma_f32_16x16x32_bf16 v[24:27], v[178:181], v[68:71], v[24:27]
	global_load_lds_dwordx4 v[148:149], off
	v_mfma_f32_16x16x32_bf16 v[20:23], v[174:177], v[68:71], v[20:23]
	v_add_u32_e32 v178, s1, v243
	v_mfma_f32_16x16x32_bf16 v[24:27], v[170:173], v[72:75], v[24:27]
	v_add_u32_e32 v170, s1, v242
	s_add_i32 s1, s0, 1
	s_cmp_lg_u32 s0, 4
	v_mfma_f32_16x16x32_bf16 v[20:23], v[166:169], v[72:75], v[20:23]
	s_cselect_b32 s0, s1, 0
	s_lshl_b32 s1, s0, 14
	v_mfma_f32_16x16x32_bf16 v[24:27], v[162:165], v[76:79], v[24:27]
	v_mfma_f32_16x16x32_bf16 v[20:23], v[158:161], v[76:79], v[20:23]
	v_mfma_f32_16x16x32_bf16 v[24:27], v[154:157], v[80:83], v[24:27]
	v_mfma_f32_16x16x32_bf16 v[20:23], v[150:153], v[80:83], v[20:23]
	ds_read_b128 v[150:153], v236 offset:33792
	ds_read_b128 v[154:157], v236 offset:32768
	ds_read_b128 v[158:161], v170
	ds_read_b128 v[162:165], v170 offset:1024
	ds_read_b128 v[166:169], v170 offset:2048
	ds_read_b128 v[170:173], v170 offset:3072
	ds_read_b128 v[174:177], v178 offset:8192
	ds_read_b128 v[178:181], v178 offset:9216
	s_waitcnt lgkmcnt(0)
	v_mfma_f32_16x16x32_bf16 v[96:99], v[174:177], v[158:161], v[96:99]
	v_mfma_f32_16x16x32_bf16 v[100:103], v[154:157], v[158:161], v[100:103]
	v_mfma_f32_16x16x32_bf16 v[104:107], v[178:181], v[158:161], v[104:107]
	v_mfma_f32_16x16x32_bf16 v[108:111], v[150:153], v[158:161], v[108:111]
	v_mfma_f32_16x16x32_bf16 v[112:115], v[174:177], v[162:165], v[112:115]
	v_mfma_f32_16x16x32_bf16 v[158:161], v[154:157], v[162:165], v[116:119]
	v_mfma_f32_16x16x32_bf16 v[182:185], v[178:181], v[162:165], v[120:123]
	v_mfma_f32_16x16x32_bf16 v[162:165], v[150:153], v[162:165], v[124:127]
	v_mfma_f32_16x16x32_bf16 v[186:189], v[174:177], v[166:169], v[128:131]
	v_mfma_f32_16x16x32_bf16 v[132:135], v[154:157], v[166:169], v[132:135]
	v_mfma_f32_16x16x32_bf16 v[120:123], v[178:181], v[166:169], v[136:139]
	v_mfma_f32_16x16x32_bf16 v[124:127], v[150:153], v[166:169], v[140:143]
	v_mfma_f32_16x16x32_bf16 v[128:131], v[174:177], v[170:173], v[144:147]
	v_add_u32_e32 v174, s33, v234
	v_add_u32_e32 v175, s33, v231
	v_add_u32_e32 v176, s33, v227
	v_mfma_f32_16x16x32_bf16 v[136:139], v[154:157], v[170:173], v[88:91]
	v_add_u32_e32 v177, s33, v229
	s_add_i32 s33, s1, 0xffffc000
	s_cmp_lg_u32 s0, 0
	v_mfma_f32_16x16x32_bf16 v[140:143], v[178:181], v[170:173], v[84:87]
	s_cselect_b32 s33, s33, 0x10000
	s_add_i32 s33, s33, 0
	s_add_i32 s33, s33, s44
	v_mfma_f32_16x16x32_bf16 v[150:153], v[150:153], v[170:173], v[92:95]
	ds_read_b64_tr_b16 v[170:171], v174
	ds_read_b64_tr_b16 v[172:173], v175
	ds_read_b64_tr_b16 v[166:167], v176
	ds_read_b64_tr_b16 v[168:169], v177
	ds_read_b64_tr_b16 v[154:155], v174 offset:2048
	ds_read_b64_tr_b16 v[156:157], v175 offset:2048
	ds_read_b64_tr_b16 v[144:145], v176 offset:2048
	ds_read_b64_tr_b16 v[146:147], v177 offset:2048
	ds_read_b64_tr_b16 v[116:117], v174 offset:4096
	ds_read_b64_tr_b16 v[118:119], v175 offset:4096
	ds_read_b64_tr_b16 v[92:93], v176 offset:4096
	ds_read_b64_tr_b16 v[94:95], v177 offset:4096
	ds_read_b64_tr_b16 v[88:89], v174 offset:6144
	ds_read_b64_tr_b16 v[90:91], v175 offset:6144
	ds_read_b64_tr_b16 v[84:85], v176 offset:6144
	ds_read_b64_tr_b16 v[86:87], v177 offset:6144
	s_waitcnt lgkmcnt(0)
	s_waitcnt vmcnt(5)
	s_barrier
	v_mfma_f32_16x16x32_bf16 v[28:31], v[166:169], v[68:71], v[28:31]
	s_add_i32 m0, s33, 0x10000
	s_add_i32 s1, s86, s1
	v_mfma_f32_16x16x32_bf16 v[32:35], v[170:173], v[68:71], v[32:35]
	s_add_i32 s33, s1, 0x2000
	v_mfma_f32_16x16x32_bf16 v[28:31], v[144:147], v[72:75], v[28:31]
	v_mfma_f32_16x16x32_bf16 v[32:35], v[154:157], v[72:75], v[32:35]
	v_mfma_f32_16x16x32_bf16 v[28:31], v[92:95], v[76:79], v[28:31]
	v_mfma_f32_16x16x32_bf16 v[32:35], v[116:119], v[76:79], v[32:35]
	v_mfma_f32_16x16x32_bf16 v[28:31], v[84:87], v[80:83], v[28:31]
	v_lshl_add_u64 v[84:85], v[148:149], 0, 64
	global_load_lds_dwordx4 v[84:85], off
	v_mfma_f32_16x16x32_bf16 v[32:35], v[88:91], v[80:83], v[32:35]
	v_add_u32_e32 v88, s1, v242
	ds_read_b128 v[154:157], v236 offset:41984
	ds_read_b128 v[166:169], v236 offset:40960
	ds_read_b128 v[84:87], v88
	ds_read_b128 v[170:173], v88 offset:1024
	ds_read_b128 v[174:177], v88 offset:2048
	ds_read_b128 v[178:181], v88 offset:3072
	v_add_u32_e32 v88, s1, v243
	ds_read_b128 v[190:193], v88 offset:8192
	ds_read_b128 v[194:197], v88 offset:9216
	s_waitcnt lgkmcnt(0)
	v_mfma_f32_16x16x32_bf16 v[144:147], v[190:193], v[84:87], v[96:99]
	s_add_i32 s1, s0, 1
	s_cmp_lg_u32 s0, 4
	s_cselect_b32 s0, s1, 0
	v_mfma_f32_16x16x32_bf16 v[116:119], v[166:169], v[84:87], v[100:103]
	s_lshl_b32 s1, s0, 14
	v_mfma_f32_16x16x32_bf16 v[104:107], v[194:197], v[84:87], v[104:107]
	v_mfma_f32_16x16x32_bf16 v[84:87], v[154:157], v[84:87], v[108:111]
	v_mfma_f32_16x16x32_bf16 v[88:91], v[190:193], v[170:173], v[112:115]
	v_mfma_f32_16x16x32_bf16 v[92:95], v[166:169], v[170:173], v[158:161]
	v_mfma_f32_16x16x32_bf16 v[96:99], v[194:197], v[170:173], v[182:185]
	v_mfma_f32_16x16x32_bf16 v[100:103], v[154:157], v[170:173], v[162:165]
	s_nop 1
	v_add_u32_e32 v182, s33, v234
	v_add_u32_e32 v183, s33, v231
	v_add_u32_e32 v184, s33, v227
	v_mfma_f32_16x16x32_bf16 v[108:111], v[190:193], v[174:177], v[186:189]
	v_add_u32_e32 v185, s33, v229
	s_add_i32 s33, s1, 0xffffc000
	s_cmp_lg_u32 s0, 0
	v_mfma_f32_16x16x32_bf16 v[112:115], v[166:169], v[174:177], v[132:135]
	s_cselect_b32 s33, s33, 0x10000
	s_add_i32 s33, s33, 0
	s_add_i32 s33, s33, s44
	v_mfma_f32_16x16x32_bf16 v[120:123], v[194:197], v[174:177], v[120:123]
	s_add_i32 m0, s33, 0x10000
	s_add_i32 s1, s86, s1
	s_add_i32 s33, s1, 0x2000
	v_mfma_f32_16x16x32_bf16 v[124:127], v[154:157], v[174:177], v[124:127]
	v_mfma_f32_16x16x32_bf16 v[128:131], v[190:193], v[178:181], v[128:131]
	v_mfma_f32_16x16x32_bf16 v[132:135], v[166:169], v[178:181], v[136:139]
	v_mfma_f32_16x16x32_bf16 v[136:139], v[194:197], v[178:181], v[140:143]
	v_mfma_f32_16x16x32_bf16 v[140:143], v[154:157], v[178:181], v[150:153]
	ds_read_b64_tr_b16 v[178:179], v182
	ds_read_b64_tr_b16 v[180:181], v183
	ds_read_b64_tr_b16 v[174:175], v184
	ds_read_b64_tr_b16 v[176:177], v185
	ds_read_b64_tr_b16 v[170:171], v182 offset:2048
	ds_read_b64_tr_b16 v[172:173], v183 offset:2048
	ds_read_b64_tr_b16 v[166:167], v184 offset:2048
	ds_read_b64_tr_b16 v[168:169], v185 offset:2048
	ds_read_b64_tr_b16 v[162:163], v182 offset:4096
	ds_read_b64_tr_b16 v[164:165], v183 offset:4096
	ds_read_b64_tr_b16 v[158:159], v184 offset:4096
	ds_read_b64_tr_b16 v[160:161], v185 offset:4096
	ds_read_b64_tr_b16 v[154:155], v182 offset:6144
	ds_read_b64_tr_b16 v[156:157], v183 offset:6144
	ds_read_b64_tr_b16 v[150:151], v184 offset:6144
	ds_read_b64_tr_b16 v[152:153], v185 offset:6144
	s_waitcnt lgkmcnt(0)
	s_waitcnt vmcnt(4)
	s_barrier
; template <int VAR  >
; __device__ __forceinline__ void ret_core_mfma(const bf16* P, const bf16* VT, const float* decay_logit  , bf16* YF, bf16* YB, float* PT, LAS unsigned char* lds, const int tid, const int bid, const int G) {
;     ...
;             for (int ks = 0; ks < 8; ++ks) {
;                 if (ks < 4) { if (c == 0) RC_WAITV(6); else RC_WAITV(14); } else if (ks == 4) RC_WAITV(6); else if (ks == 5) RC_WAITV(5); else if (ks == 6) RC_WAITV(4); else RC_WAITV(3);
;                 RC_BAR();
;                 { const int s4 = RC_PREV(slot);
;                   if (ks + 4 < 12) RC_ISSUE(ks + 4, tok0, s4); else RC_ISSUE(ks + 4 - 12, tokn, s4); }
;                 bf16x8v At[4], Bk[2], Bs[2];
;                 const LAS unsigned char* sq = lds + RC_RG + slot * 16384;
; #pragma unroll
;                 for (int m = 0; m < 4; ++m) At[m] = *(const LAS bf16x8v*)(sq + aoff + m * 1024);
; #pragma unroll
;                 for (int n = 0; n < 2; ++n) { Bk[n] = *(const LAS bf16x8v*)(sq + 8192 + boff + n * 1024); Bs[n] = *(const LAS bf16x8v*)(lds + RC_ST + ks * 8192 + boff + n * 1024); }
; #pragma unroll
;                 for (int m = 0; m < 4; ++m)
; #pragma unroll
;                     for (int n = 0; n < 2; ++n) { accA[m][n] = RC_MFMA(Bk[n], At[m], accA[m][n]); accY[m][n] = RC_MFMA(Bs[n], At[m], accY[m][n]); }
;                 { const unsigned kb = (unsigned)(size_t)(sq + 8192);
;                   const unsigned a0 = kb + trA, a1 = kb + trB, b0 = kb + (trA ^ 32u), b1 = kb + (trB ^ 32u);
;                   v2u l0, h0, l1, h1, l2, h2, l3, h3, p0, q0, p1, q1, p2, q2, p3, q3;
;                   asm volatile("ds_read_b64_tr_b16 %0, %16\n\tds_read_b64_tr_b16 %1, %17\n\tds_read_b64_tr_b16 %8, %18\n\tds_read_b64_tr_b16 %9, %19\n\t"
;                                "ds_read_b64_tr_b16 %2, %16 offset:2048\n\tds_read_b64_tr_b16 %3, %17 offset:2048\n\tds_read_b64_tr_b16 %10, %18 offset:2048\n\tds_read_b64_tr_b16 %11, %19 offset:2048\n\t"
;                                "ds_read_b64_tr_b16 %4, %16 offset:4096\n\tds_read_b64_tr_b16 %5, %17 offset:4096\n\tds_read_b64_tr_b16 %12, %18 offset:4096\n\tds_read_b64_tr_b16 %13, %19 offset:4096\n\t"
;                                "ds_read_b64_tr_b16 %6, %16 offset:6144\n\tds_read_b64_tr_b16 %7, %17 offset:6144\n\tds_read_b64_tr_b16 %14, %18 offset:6144\n\tds_read_b64_tr_b16 %15, %19 offset:6144\n\ts_waitcnt lgkmcnt(0)"
	v_mfma_f32_16x16x32_bf16 v[44:47], v[174:177], v[68:71], v[44:47]
	v_mfma_f32_16x16x32_bf16 v[48:51], v[178:181], v[68:71], v[48:51]
	v_add_u32_e32 v178, s1, v243
	v_mfma_f32_16x16x32_bf16 v[44:47], v[166:169], v[72:75], v[44:47]
	v_mfma_f32_16x16x32_bf16 v[48:51], v[170:173], v[72:75], v[48:51]
	v_add_u32_e32 v170, s1, v242
	s_add_i32 s1, s0, 1
	s_cmp_lg_u32 s0, 4
	v_mfma_f32_16x16x32_bf16 v[44:47], v[158:161], v[76:79], v[44:47]
	v_mfma_f32_16x16x32_bf16 v[48:51], v[162:165], v[76:79], v[48:51]
	v_mfma_f32_16x16x32_bf16 v[44:47], v[150:153], v[80:83], v[44:47]
	v_lshl_add_u64 v[150:151], v[148:149], 0, s[66:67]
	global_load_lds_dwordx4 v[150:151], off
	v_mfma_f32_16x16x32_bf16 v[48:51], v[154:157], v[80:83], v[48:51]
	ds_read_b128 v[150:153], v236 offset:50176
	ds_read_b128 v[154:157], v236 offset:49152
	ds_read_b128 v[158:161], v170
	ds_read_b128 v[162:165], v170 offset:1024
	ds_read_b128 v[166:169], v170 offset:2048
	ds_read_b128 v[170:173], v170 offset:3072
	ds_read_b128 v[174:177], v178 offset:8192
	ds_read_b128 v[178:181], v178 offset:9216
	s_waitcnt lgkmcnt(0)
	v_mfma_f32_16x16x32_bf16 v[144:147], v[174:177], v[158:161], v[144:147]
	v_mfma_f32_16x16x32_bf16 v[116:119], v[154:157], v[158:161], v[116:119]
	v_mfma_f32_16x16x32_bf16 v[104:107], v[178:181], v[158:161], v[104:107]
	v_mfma_f32_16x16x32_bf16 v[84:87], v[150:153], v[158:161], v[84:87]
	v_mfma_f32_16x16x32_bf16 v[88:91], v[174:177], v[162:165], v[88:91]
	v_mfma_f32_16x16x32_bf16 v[92:95], v[154:157], v[162:165], v[92:95]
	v_mfma_f32_16x16x32_bf16 v[96:99], v[178:181], v[162:165], v[96:99]
	v_mfma_f32_16x16x32_bf16 v[158:161], v[150:153], v[162:165], v[100:103]
	v_mfma_f32_16x16x32_bf16 v[108:111], v[174:177], v[166:169], v[108:111]
	v_mfma_f32_16x16x32_bf16 v[162:165], v[154:157], v[166:169], v[112:115]
	v_mfma_f32_16x16x32_bf16 v[182:185], v[178:181], v[166:169], v[120:123]
	v_mfma_f32_16x16x32_bf16 v[166:169], v[150:153], v[166:169], v[124:127]
	v_mfma_f32_16x16x32_bf16 v[174:177], v[174:177], v[170:173], v[128:131]
	v_mfma_f32_16x16x32_bf16 v[154:157], v[154:157], v[170:173], v[132:135]
	v_mfma_f32_16x16x32_bf16 v[178:181], v[178:181], v[170:173], v[136:139]
	v_mfma_f32_16x16x32_bf16 v[150:153], v[150:153], v[170:173], v[140:143]
	v_add_u32_e32 v170, s33, v234
	v_add_u32_e32 v171, s33, v231
	v_add_u32_e32 v172, s33, v227
	v_add_u32_e32 v173, s33, v229
	ds_read_b64_tr_b16 v[140:141], v170
	ds_read_b64_tr_b16 v[142:143], v171
	ds_read_b64_tr_b16 v[136:137], v172
	ds_read_b64_tr_b16 v[138:139], v173
	ds_read_b64_tr_b16 v[132:133], v170 offset:2048
	ds_read_b64_tr_b16 v[134:135], v171 offset:2048
	ds_read_b64_tr_b16 v[128:129], v172 offset:2048
	ds_read_b64_tr_b16 v[130:131], v173 offset:2048
	ds_read_b64_tr_b16 v[124:125], v170 offset:4096
	ds_read_b64_tr_b16 v[126:127], v171 offset:4096
	ds_read_b64_tr_b16 v[120:121], v172 offset:4096
	ds_read_b64_tr_b16 v[122:123], v173 offset:4096
	ds_read_b64_tr_b16 v[112:113], v170 offset:6144
	ds_read_b64_tr_b16 v[114:115], v171 offset:6144
	ds_read_b64_tr_b16 v[100:101], v172 offset:6144
	ds_read_b64_tr_b16 v[102:103], v173 offset:6144
	s_waitcnt lgkmcnt(0)
	s_cselect_b32 s33, s1, 0
	v_mfma_f32_16x16x32_bf16 v[56:59], v[136:139], v[68:71], v[56:59]
	s_lshl_b32 s0, s33, 14
	s_add_i32 s1, s0, 0xffffc000
	s_cmp_lg_u32 s33, 0
	v_mfma_f32_16x16x32_bf16 v[52:55], v[140:143], v[68:71], v[52:55]
	s_cselect_b32 s1, s1, 0x10000
	s_add_i32 s1, s1, 0
	s_waitcnt vmcnt(3)
	v_mfma_f32_16x16x32_bf16 v[56:59], v[128:131], v[72:75], v[56:59]
	s_add_i32 s1, s1, s44
	s_barrier
	v_mfma_f32_16x16x32_bf16 v[52:55], v[132:135], v[72:75], v[52:55]
	s_add_i32 m0, s1, 0x10000
	s_add_i32 s0, s86, s0
	v_mfma_f32_16x16x32_bf16 v[56:59], v[120:123], v[76:79], v[56:59]
	v_add_u32_e32 v120, s0, v242
	s_add_i32 s1, s0, 0x2000
	s_add_i32 s38, s33, 1
	v_mfma_f32_16x16x32_bf16 v[52:55], v[124:127], v[76:79], v[52:55]
	s_cmp_lg_u32 s33, 4
	v_mfma_f32_16x16x32_bf16 v[56:59], v[100:103], v[80:83], v[56:59]
	v_lshl_add_u64 v[100:101], v[148:149], 0, s[16:17]
	global_load_lds_dwordx4 v[100:101], off
	v_mfma_f32_16x16x32_bf16 v[52:55], v[112:115], v[80:83], v[52:55]
	ds_read_b128 v[170:173], v236 offset:58368
	ds_read_b128 v[186:189], v236 offset:57344
	ds_read_b128 v[100:103], v120
	ds_read_b128 v[112:115], v120 offset:1024
	ds_read_b128 v[190:193], v120 offset:2048
	ds_read_b128 v[194:197], v120 offset:3072
	v_add_u32_e32 v120, s0, v243
	ds_read_b128 v[202:205], v120 offset:8192
	ds_read_b128 v[208:211], v120 offset:9216
	s_waitcnt lgkmcnt(0)
	v_mfma_f32_16x16x32_bf16 v[140:143], v[202:205], v[100:103], v[144:147]
	v_mfma_f32_16x16x32_bf16 v[238:241], v[186:189], v[100:103], v[116:119]
	v_mfma_f32_16x16x32_bf16 v[132:135], v[208:211], v[100:103], v[104:107]
	v_mfma_f32_16x16x32_bf16 v[136:139], v[170:173], v[100:103], v[84:87]
	v_mfma_f32_16x16x32_bf16 v[104:107], v[202:205], v[112:115], v[88:91]
	v_mfma_f32_16x16x32_bf16 v[100:103], v[186:189], v[112:115], v[92:95]
	v_mfma_f32_16x16x32_bf16 v[124:127], v[208:211], v[112:115], v[96:99]
	v_mfma_f32_16x16x32_bf16 v[128:131], v[170:173], v[112:115], v[158:161]
	v_mfma_f32_16x16x32_bf16 v[120:123], v[186:189], v[190:193], v[162:165]
	v_mfma_f32_16x16x32_bf16 v[116:119], v[170:173], v[190:193], v[166:169]
	v_mfma_f32_16x16x32_bf16 v[92:95], v[202:205], v[194:197], v[174:177]
	v_mfma_f32_16x16x32_bf16 v[96:99], v[186:189], v[194:197], v[154:157]
	s_nop 1
	v_add_u32_e32 v176, s1, v234
	v_add_u32_e32 v177, s1, v231
	v_mov_b32_e32 v231, v3
	v_mfma_f32_16x16x32_bf16 v[84:87], v[208:211], v[194:197], v[178:181]
	v_mfma_f32_16x16x32_bf16 v[88:91], v[170:173], v[194:197], v[150:153]
	s_nop 1
	v_add_u32_e32 v178, s1, v227
	v_add_u32_e32 v179, s1, v229
	ds_read_b64_tr_b16 v[172:173], v176
	ds_read_b64_tr_b16 v[174:175], v177
	ds_read_b64_tr_b16 v[168:169], v178
	ds_read_b64_tr_b16 v[170:171], v179
	ds_read_b64_tr_b16 v[164:165], v176 offset:2048
	ds_read_b64_tr_b16 v[166:167], v177 offset:2048
	ds_read_b64_tr_b16 v[160:161], v178 offset:2048
	ds_read_b64_tr_b16 v[162:163], v179 offset:2048
	ds_read_b64_tr_b16 v[156:157], v176 offset:4096
	ds_read_b64_tr_b16 v[158:159], v177 offset:4096
	ds_read_b64_tr_b16 v[152:153], v178 offset:4096
	ds_read_b64_tr_b16 v[154:155], v179 offset:4096
	ds_read_b64_tr_b16 v[148:149], v176 offset:6144
	ds_read_b64_tr_b16 v[150:151], v177 offset:6144
	ds_read_b64_tr_b16 v[144:145], v178 offset:6144
	ds_read_b64_tr_b16 v[146:147], v179 offset:6144
	s_waitcnt lgkmcnt(0)
; #define LAS __attribute__((address_space(3)))
; template <int VAR  >
; __device__ __forceinline__ void ret_core_mfma(const bf16* P, const bf16* VT, const float* decay_logit  , bf16* YF, bf16* YB, float* PT, LAS unsigned char* lds, const int tid, const int bid, const int G) {
;     ...
; #pragma unroll
;             for (int m = 0; m < 4; ++m)
; #pragma unroll
;                 for (int n = 0; n < 2; ++n) { const int i = 64 * wr + 16 * m + frc;
;                     const float qdf = *(const LAS float*)(lds + RC_TB + 1536 + i * 4), rwf = *(const LAS float*)(lds + RC_TB + 512 + i * 4);
;                     const f32x4 clf = *(const LAS f32x4*)(lds + RC_TB + 1024 + (32 * wc + 16 * n + 4 * fqc) * 4);
;                     accY[m][n] = accY[m][n] * qdf;
; #pragma unroll
;                     for (int ii = 0; ii < 4; ++ii) { const int j = 32 * wc + 16 * n + 4 * fqc + ii; const int dd = dir ? j - i : i - j;
;                         accA[m][n][ii] = dd >= 0 ? accA[m][n][ii] * (rwf * clf[ii]) : 0.f; } }
	v_mfma_f32_16x16x32_bf16 v[112:115], v[202:205], v[190:193], v[108:111]
	v_ashrrev_i32_e32 v229, 31, v228
	v_ashrrev_i32_e32 v227, 31, v226
	v_mfma_f32_16x16x32_bf16 v[60:63], v[172:175], v[68:71], v[60:63]
	v_mfma_f32_16x16x32_bf16 v[64:67], v[168:171], v[68:71], v[64:67]
	v_mfma_f32_16x16x32_bf16 v[60:63], v[164:167], v[72:75], v[60:63]
	v_mfma_f32_16x16x32_bf16 v[64:67], v[160:163], v[72:75], v[64:67]
	v_mfma_f32_16x16x32_bf16 v[60:63], v[156:159], v[76:79], v[60:63]
	v_mfma_f32_16x16x32_bf16 v[64:67], v[152:155], v[76:79], v[64:67]
	v_mfma_f32_16x16x32_bf16 v[60:63], v[148:151], v[80:83], v[60:63]
	v_or_b32_e32 v149, s77, v2
	v_lshlrev_b32_e32 v68, 2, v149
	v_add_u32_e32 v69, s35, v68
	v_mfma_f32_16x16x32_bf16 v[64:67], v[144:147], v[80:83], v[64:67]
	v_lshl_add_u32 v144, v215, 2, s82
	ds_read_b32 v72, v69
	v_add_u32_e32 v68, s64, v68
	ds_read_b32 v150, v68
	v_lshl_add_u32 v68, v144, 2, s65
	ds_read_b128 v[76:79], v68
	s_waitcnt lgkmcnt(0)
	v_pk_mul_f32 v[70:71], v[240:241], v[72:73] op_sel_hi:[1,0]
	v_pk_mul_f32 v[68:69], v[238:239], v[72:73] op_sel_hi:[1,0]
	v_sub_u32_e32 v73, v144, v149
	v_sub_u32_e32 v74, v149, v144
	v_cndmask_b32_e64 v73, v73, v74, s[4:5]
	v_cmp_lt_i32_e32 vcc, -1, v73
	v_mul_f32_e32 v73, v150, v76
	v_mul_f32_e32 v73, v140, v73
	v_or_b32_e32 v145, 1, v144
	v_cndmask_b32_e32 v140, 0, v73, vcc
	v_sub_u32_e32 v73, v145, v149
	v_sub_u32_e32 v74, v149, v145
	v_cndmask_b32_e64 v73, v73, v74, s[4:5]
	v_cmp_lt_i32_e64 s[0:1], -1, v73
	v_mul_f32_e32 v73, v150, v77
	v_mul_f32_e32 v73, v141, v73
	v_or_b32_e32 v146, 2, v144
	v_cndmask_b32_e64 v141, 0, v73, s[0:1]
	v_sub_u32_e32 v73, v146, v149
	v_sub_u32_e32 v74, v149, v146
	v_cndmask_b32_e64 v73, v73, v74, s[4:5]
	v_cmp_lt_i32_e64 s[0:1], -1, v73
	v_mul_f32_e32 v73, v150, v78
	v_mul_f32_e32 v73, v142, v73
	v_or_b32_e32 v147, 3, v144
	v_cndmask_b32_e64 v142, 0, v73, s[0:1]
	v_sub_u32_e32 v73, v147, v149
	v_sub_u32_e32 v74, v149, v147
	v_cndmask_b32_e64 v73, v73, v74, s[4:5]
	v_cmp_lt_i32_e64 s[0:1], -1, v73
	v_mul_f32_e32 v73, v150, v79
	v_mul_f32_e32 v73, v143, v73
	v_add_u32_e32 v148, 16, v144
	v_cndmask_b32_e64 v143, 0, v73, s[0:1]
	v_lshl_add_u32 v73, v148, 2, s65
	ds_read_b128 v[80:83], v73
	v_pk_mul_f32 v[74:75], v[138:139], v[72:73] op_sel_hi:[1,0]
	v_pk_mul_f32 v[72:73], v[136:137], v[72:73] op_sel_hi:[1,0]
	v_sub_u32_e32 v136, v148, v149
	v_sub_u32_e32 v137, v149, v148
	v_cndmask_b32_e64 v136, v136, v137, s[4:5]
	v_cmp_lt_i32_e64 s[0:1], -1, v136
	s_waitcnt lgkmcnt(0)
	v_mul_f32_e32 v136, v150, v80
	v_add_u32_e32 v138, 17, v144
	v_mul_f32_e32 v132, v132, v136
	v_sub_u32_e32 v136, v138, v149
	v_sub_u32_e32 v137, v149, v138
	v_cndmask_b32_e64 v136, v136, v137, s[4:5]
	v_cndmask_b32_e64 v132, 0, v132, s[0:1]
	v_cmp_lt_i32_e64 s[0:1], -1, v136
	v_mul_f32_e32 v136, v150, v81
	v_add_u32_e32 v137, 18, v144
	v_mul_f32_e32 v133, v133, v136
	v_sub_u32_e32 v136, v137, v149
	v_sub_u32_e32 v139, v149, v137
	v_cndmask_b32_e64 v136, v136, v139, s[4:5]
	v_cndmask_b32_e64 v133, 0, v133, s[0:1]
	v_cmp_lt_i32_e64 s[0:1], -1, v136
	v_mul_f32_e32 v136, v150, v82
	v_mul_f32_e32 v134, v134, v136
	v_add_u32_e32 v136, 19, v144
	v_sub_u32_e32 v139, v136, v149
	v_sub_u32_e32 v151, v149, v136
	v_cndmask_b32_e64 v139, v139, v151, s[4:5]
	v_cndmask_b32_e64 v134, 0, v134, s[0:1]
	v_cmp_lt_i32_e64 s[0:1], -1, v139
	v_mul_f32_e32 v139, v150, v83
	v_or_b32_e32 v153, 16, v149
	v_mul_f32_e32 v135, v135, v139
	v_lshlrev_b32_e32 v139, 2, v153
	v_add_u32_e32 v150, s35, v139
	v_add_u32_e32 v139, s64, v139
	ds_read_b32 v154, v150
	ds_read_b32 v155, v139
	v_sub_u32_e32 v139, v144, v153
	v_sub_u32_e32 v150, v153, v144
	v_cndmask_b32_e64 v139, v139, v150, s[4:5]
	v_cndmask_b32_e64 v135, 0, v135, s[0:1]
	v_cmp_lt_i32_e64 s[0:1], -1, v139
	s_waitcnt lgkmcnt(0)
	v_mul_f32_e32 v139, v76, v155
	v_mul_f32_e32 v104, v104, v139
	v_cndmask_b32_e64 v139, 0, v104, s[0:1]
	v_sub_u32_e32 v104, v145, v153
	v_sub_u32_e32 v150, v153, v145
	v_cndmask_b32_e64 v104, v104, v150, s[4:5]
	v_cmp_lt_i32_e64 s[0:1], -1, v104
	v_mul_f32_e32 v104, v77, v155
	v_mul_f32_e32 v104, v105, v104
	v_cndmask_b32_e64 v150, 0, v104, s[0:1]
	v_sub_u32_e32 v104, v146, v153
	v_sub_u32_e32 v105, v153, v146
	v_cndmask_b32_e64 v104, v104, v105, s[4:5]
	v_cmp_lt_i32_e64 s[0:1], -1, v104
	v_mul_f32_e32 v104, v78, v155
	v_mul_f32_e32 v104, v106, v104
	v_cndmask_b32_e64 v151, 0, v104, s[0:1]
	v_sub_u32_e32 v104, v147, v153
	v_sub_u32_e32 v105, v153, v147
	v_cndmask_b32_e64 v104, v104, v105, s[4:5]
	v_cmp_lt_i32_e64 s[0:1], -1, v104
	v_mul_f32_e32 v104, v79, v155
	v_mul_f32_e32 v104, v107, v104
	v_cndmask_b32_e64 v152, 0, v104, s[0:1]
	v_pk_mul_f32 v[104:105], v[128:129], v[154:155] op_sel_hi:[1,0]
	v_mul_f32_e32 v128, v80, v155
	v_mul_f32_e32 v124, v124, v128
	v_cndmask_b32_e32 v128, 0, v124, vcc
	v_sub_u32_e32 v124, v138, v153
	v_sub_u32_e32 v129, v153, v138
	v_cndmask_b32_e64 v124, v124, v129, s[4:5]
	v_cmp_lt_i32_e32 vcc, -1, v124
	v_mul_f32_e32 v124, v81, v155
	v_mul_f32_e32 v124, v125, v124
	v_cndmask_b32_e32 v125, 0, v124, vcc
	v_sub_u32_e32 v124, v137, v153
	v_sub_u32_e32 v129, v153, v137
	v_cndmask_b32_e64 v124, v124, v129, s[4:5]
	v_cmp_lt_i32_e32 vcc, -1, v124
	v_mul_f32_e32 v124, v82, v155
	v_mul_f32_e32 v124, v126, v124
	v_cndmask_b32_e32 v126, 0, v124, vcc
	v_sub_u32_e32 v124, v136, v153
	v_sub_u32_e32 v129, v153, v136
	v_cndmask_b32_e64 v124, v124, v129, s[4:5]
	v_pk_mul_f32 v[102:103], v[102:103], v[154:155] op_sel_hi:[1,0]
	v_pk_mul_f32 v[100:101], v[100:101], v[154:155] op_sel_hi:[1,0]
	v_pk_mul_f32 v[106:107], v[130:131], v[154:155] op_sel_hi:[1,0]
	v_cmp_lt_i32_e32 vcc, -1, v124
	v_mul_f32_e32 v124, v83, v155
	v_or_b32_e32 v154, 32, v149
	v_mul_f32_e32 v124, v127, v124
	v_lshlrev_b32_e32 v129, 2, v154
	v_cndmask_b32_e32 v127, 0, v124, vcc
	v_add_u32_e32 v124, s35, v129
	v_add_u32_e32 v129, s64, v129
	ds_read_b32 v124, v124
	ds_read_b32 v155, v129
	v_sub_u32_e32 v129, v144, v154
	v_sub_u32_e32 v130, v154, v144
	v_cndmask_b32_e64 v129, v129, v130, s[4:5]
	v_cmp_lt_i32_e32 vcc, -1, v129
	s_waitcnt lgkmcnt(0)
; #define LAS __attribute__((address_space(3)))
; __device__ __forceinline__ unsigned cvtpk(float lo, float hi) { f32x2_t v = {lo, hi}; bf16x2_t b = __builtin_convertvector(v, bf16x2_t); return __builtin_bit_cast(unsigned, b); }
; #define RC_WAITL() asm volatile("s_waitcnt lgkmcnt(0)" ::: "memory")
; #define RC_BAR() do { asm volatile("" ::: "memory"); __builtin_amdgcn_s_barrier(); asm volatile("" ::: "memory"); } while (0)
; template <int VAR  >
; __device__ __forceinline__ void ret_core_mfma(const bf16* P, const bf16* VT, const float* decay_logit  , bf16* YF, bf16* YB, float* PT, LAS unsigned char* lds, const int tid, const int bid, const int G) {
;     ...
; #pragma unroll
;             for (int m = 0; m < 4; ++m)
; #pragma unroll
;                 for (int n = 0; n < 2; ++n) { const int i = 64 * wr + 16 * m + frc;
;                     const float qdf = *(const LAS float*)(lds + RC_TB + 1536 + i * 4), rwf = *(const LAS float*)(lds + RC_TB + 512 + i * 4);
;                     const f32x4 clf = *(const LAS f32x4*)(lds + RC_TB + 1024 + (32 * wc + 16 * n + 4 * fqc) * 4);
;                     accY[m][n] = accY[m][n] * qdf;
; #pragma unroll
;                     for (int ii = 0; ii < 4; ++ii) { const int j = 32 * wc + 16 * n + 4 * fqc + ii; const int dd = dir ? j - i : i - j;
;                         accA[m][n][ii] = dd >= 0 ? accA[m][n][ii] * (rwf * clf[ii]) : 0.f; } }
;             RC_BAR();
; #pragma unroll
;             for (int m = 0; m < 4; ++m)
; #pragma unroll
;                 for (int n = 0; n < 2; ++n) { v2u pw; pw.x = cvtpk(accA[m][n][0], accA[m][n][1]); pw.y = cvtpk(accA[m][n][2], accA[m][n][3]);
;                     *(LAS v2u*)(lds + RC_ST + wc * 8192 + (4 * wr + m) * 1024 + sl_swz(frc * 64 + (16 * n + 4 * fqc) * 2)) = pw; }
; #pragma unroll
;             for (int js = 0; js < 4; ++js) vnx[js] = *(const v4u*)(vown + tokn + 32 * js + zo);
;             RC_WAITL();
	v_mul_f32_e32 v129, v76, v155
	v_mul_f32_e32 v112, v112, v129
	v_cndmask_b32_e32 v129, 0, v112, vcc
	v_sub_u32_e32 v112, v145, v154
	v_sub_u32_e32 v130, v154, v145
	v_cndmask_b32_e64 v112, v112, v130, s[4:5]
	v_cmp_lt_i32_e32 vcc, -1, v112
	v_mul_f32_e32 v112, v77, v155
	v_mul_f32_e32 v112, v113, v112
	v_cndmask_b32_e32 v130, 0, v112, vcc
	v_sub_u32_e32 v112, v146, v154
	v_sub_u32_e32 v113, v154, v146
	v_cndmask_b32_e64 v112, v112, v113, s[4:5]
	v_cmp_lt_i32_e32 vcc, -1, v112
	v_mul_f32_e32 v112, v78, v155
	v_mul_f32_e32 v112, v114, v112
	v_cndmask_b32_e32 v131, 0, v112, vcc
	v_sub_u32_e32 v112, v147, v154
	v_sub_u32_e32 v113, v154, v147
	v_cndmask_b32_e64 v112, v112, v113, s[4:5]
	v_cmp_lt_i32_e32 vcc, -1, v112
	v_mul_f32_e32 v112, v79, v155
	v_mfma_f32_16x16x32_bf16 v[108:111], v[208:211], v[190:193], v[182:185]
	v_mul_f32_e32 v112, v115, v112
	v_cndmask_b32_e32 v153, 0, v112, vcc
	v_pk_mul_f32 v[112:113], v[116:117], v[124:125] op_sel_hi:[1,0]
	v_sub_u32_e32 v116, v148, v154
	v_sub_u32_e32 v117, v154, v148
	v_cndmask_b32_e64 v116, v116, v117, s[4:5]
	v_cmp_lt_i32_e32 vcc, -1, v116
	v_mul_f32_e32 v116, v80, v155
	v_mul_f32_e32 v108, v108, v116
	v_sub_u32_e32 v116, v138, v154
	v_sub_u32_e32 v117, v154, v138
	v_cndmask_b32_e64 v116, v116, v117, s[4:5]
	v_cndmask_b32_e32 v108, 0, v108, vcc
	v_cmp_lt_i32_e32 vcc, -1, v116
	v_mul_f32_e32 v116, v81, v155
	v_mul_f32_e32 v109, v109, v116
	v_sub_u32_e32 v116, v137, v154
	v_sub_u32_e32 v117, v154, v137
	v_cndmask_b32_e64 v116, v116, v117, s[4:5]
	v_cndmask_b32_e32 v109, 0, v109, vcc
	v_cmp_lt_i32_e32 vcc, -1, v116
	v_mul_f32_e32 v116, v82, v155
	v_mul_f32_e32 v110, v110, v116
	v_sub_u32_e32 v116, v136, v154
	v_sub_u32_e32 v117, v154, v136
	v_cndmask_b32_e64 v116, v116, v117, s[4:5]
	v_or_b32_e32 v117, 48, v149
	v_pk_mul_f32 v[114:115], v[118:119], v[124:125] op_sel_hi:[1,0]
	v_cndmask_b32_e32 v110, 0, v110, vcc
	v_cmp_lt_i32_e32 vcc, -1, v116
	v_mul_f32_e32 v116, v83, v155
	v_lshlrev_b32_e32 v118, 2, v117
	v_mul_f32_e32 v111, v111, v116
	v_add_u32_e32 v116, s35, v118
	v_add_u32_e32 v118, s64, v118
	ds_read_b32 v116, v116
	ds_read_b32 v118, v118
	v_pk_mul_f32 v[122:123], v[122:123], v[124:125] op_sel_hi:[1,0]
	v_pk_mul_f32 v[120:121], v[120:121], v[124:125] op_sel_hi:[1,0]
	v_sub_u32_e32 v119, v144, v117
	v_sub_u32_e32 v124, v117, v144
	v_cndmask_b32_e64 v119, v119, v124, s[4:5]
	s_waitcnt lgkmcnt(0)
	v_mul_f32_e32 v76, v76, v118
	v_cndmask_b32_e32 v111, 0, v111, vcc
	v_cmp_lt_i32_e32 vcc, -1, v119
	v_mul_f32_e32 v76, v92, v76
	v_sub_u32_e32 v92, v117, v145
	v_cndmask_b32_e32 v119, 0, v76, vcc
	v_sub_u32_e32 v76, v145, v117
	v_cndmask_b32_e64 v76, v76, v92, s[4:5]
	v_cmp_lt_i32_e32 vcc, -1, v76
	v_mul_f32_e32 v76, v77, v118
	v_mul_f32_e32 v76, v93, v76
	v_cndmask_b32_e32 v124, 0, v76, vcc
	v_sub_u32_e32 v76, v146, v117
	v_sub_u32_e32 v77, v117, v146
	v_cndmask_b32_e64 v76, v76, v77, s[4:5]
	v_cmp_lt_i32_e32 vcc, -1, v76
	v_mul_f32_e32 v76, v78, v118
	v_mul_f32_e32 v76, v94, v76
	v_cndmask_b32_e32 v78, 0, v76, vcc
	v_sub_u32_e32 v76, v147, v117
	v_sub_u32_e32 v77, v117, v147
	v_cndmask_b32_e64 v76, v76, v77, s[4:5]
	v_cmp_lt_i32_e32 vcc, -1, v76
	v_mul_f32_e32 v76, v79, v118
	v_mul_f32_e32 v76, v95, v76
	v_cndmask_b32_e32 v79, 0, v76, vcc
	v_sub_u32_e32 v76, v148, v117
	v_sub_u32_e32 v77, v117, v148
	v_cndmask_b32_e64 v76, v76, v77, s[4:5]
	v_cmp_lt_i32_e32 vcc, -1, v76
	v_mul_f32_e32 v76, v80, v118
	v_mul_f32_e32 v76, v84, v76
	v_cndmask_b32_e32 v80, 0, v76, vcc
	v_sub_u32_e32 v76, v138, v117
	v_sub_u32_e32 v77, v117, v138
	v_cndmask_b32_e64 v76, v76, v77, s[4:5]
	v_cmp_lt_i32_e32 vcc, -1, v76
	v_mul_f32_e32 v76, v81, v118
	v_mul_f32_e32 v76, v85, v76
	v_cndmask_b32_e32 v81, 0, v76, vcc
	v_sub_u32_e32 v76, v137, v117
	v_sub_u32_e32 v77, v117, v137
	v_cndmask_b32_e64 v76, v76, v77, s[4:5]
	v_cmp_lt_i32_e32 vcc, -1, v76
	v_mul_f32_e32 v76, v82, v118
	v_mul_f32_e32 v76, v86, v76
	v_lshl_add_u32 v84, v2, 6, v226
	v_cndmask_b32_e32 v82, 0, v76, vcc
	v_sub_u32_e32 v76, v136, v117
	v_sub_u32_e32 v77, v117, v136
	v_lshrrev_b32_e32 v85, 4, v84
	v_cndmask_b32_e64 v76, v76, v77, s[4:5]
	v_and_b32_e32 v85, 32, v85
	v_cmp_lt_i32_e32 vcc, -1, v76
	v_mul_f32_e32 v76, v83, v118
	v_xad_u32 v85, v85, v84, s83
	v_add_u32_e32 v84, 32, v84
	v_mul_f32_e32 v76, v87, v76
	v_lshrrev_b32_e32 v86, 4, v84
	v_cndmask_b32_e32 v83, 0, v76, vcc
	v_cvt_pk_bf16_f32 v76, v140, v141
	v_cvt_pk_bf16_f32 v77, v142, v143
	v_and_b32_e32 v86, 32, v86
	s_barrier
	ds_write_b64 v85, v[76:77]
	v_cvt_pk_bf16_f32 v76, v132, v133
	v_cvt_pk_bf16_f32 v77, v134, v135
	v_xad_u32 v84, v86, v84, s83
	ds_write_b64 v84, v[76:77]
	v_cvt_pk_bf16_f32 v76, v139, v150
	v_cvt_pk_bf16_f32 v77, v151, v152
	ds_write_b64 v85, v[76:77] offset:1024
	v_cvt_pk_bf16_f32 v76, v128, v125
	v_cvt_pk_bf16_f32 v77, v126, v127
	ds_write_b64 v84, v[76:77] offset:1024
	v_cvt_pk_bf16_f32 v76, v129, v130
	v_cvt_pk_bf16_f32 v77, v131, v153
	ds_write_b64 v85, v[76:77] offset:2048
	v_cvt_pk_bf16_f32 v76, v108, v109
	v_cvt_pk_bf16_f32 v77, v110, v111
	s_cselect_b32 s0, s38, 0
	ds_write_b64 v84, v[76:77] offset:2048
	v_cvt_pk_bf16_f32 v76, v119, v124
	v_cvt_pk_bf16_f32 v77, v78, v79
	s_lshl_b32 s40, s7, 7
	ds_write_b64 v85, v[76:77] offset:3072
	v_cvt_pk_bf16_f32 v76, v80, v81
	v_cvt_pk_bf16_f32 v77, v82, v83
	s_ashr_i32 s41, s40, 31
	s_lshl_b32 s1, s0, 14
	ds_write_b64 v84, v[76:77] offset:3072
	v_lshl_add_u64 v[76:77], s[40:41], 1, v[222:223]
	s_lshl_b64 s[40:41], s[40:41], 12
	s_add_i32 s7, s1, 0xc000
	v_lshl_add_u64 v[80:81], v[228:229], 1, v[76:77]
	s_cmp_lg_u32 s0, 0
	v_pk_mul_f32 v[94:95], v[90:91], v[116:117] op_sel_hi:[1,0]
	v_pk_mul_f32 v[92:93], v[88:89], v[116:117] op_sel_hi:[1,0]
	global_load_dwordx4 v[88:91], v[80:81], off
	global_load_dwordx4 v[84:87], v[80:81], off offset:64
	global_load_dwordx4 v[76:79], v[80:81], off offset:128
	s_nop 0
	global_load_dwordx4 v[80:83], v[80:81], off offset:192
	s_waitcnt lgkmcnt(0)
	s_cselect_b32 s7, s7, 0x20000
	s_waitcnt vmcnt(7)
	s_add_i32 s7, s45, s7
	s_barrier
; #define LAS __attribute__((address_space(3)))
; #define RC_WAITV(n) asm volatile("s_waitcnt vmcnt(" #n ")" ::: "memory")
; #define RC_WAITL() asm volatile("s_waitcnt lgkmcnt(0)" ::: "memory")
; #define RC_BAR() do { asm volatile("" ::: "memory"); __builtin_amdgcn_s_barrier(); asm volatile("" ::: "memory"); } while (0)
; #define RC_MFMA(b, a, c) __builtin_amdgcn_mfma_f32_16x16x32_bf16((b), (a), (c), 0, 0, 0)
; #define RC_ISSUE(st, tk, sl) do { if ((st) < 8) { const size_t to_ = (size_t)(tk) * RQK + 32 * (st); RC_DMA(qsrc + to_, RC_RG + (sl) * 16384 + w * 1024); RC_DMA(ksrc + to_, RC_RG + (sl) * 16384 + 8192 + w * 1024); } \
;                                   else RC_DMA(vsrc + (tk) + 32 * ((st) - 8), RC_RG + (sl) * 16384 + w * 1024); } while (0)
; template <int VAR  >
; __device__ __forceinline__ void ret_core_mfma(const bf16* P, const bf16* VT, const float* decay_logit  , bf16* YF, bf16* YB, float* PT, LAS unsigned char* lds, const int tid, const int bid, const int G) {
;     ...
; #pragma unroll
;             for (int js = 0; js < 4; ++js) {
;                 if (js == 0) RC_WAITV(7); else if (js == 1) RC_WAITV(8); else if (js == 2) RC_WAITV(9); else RC_WAITV(10);
;                 RC_BAR();
;                 { const int s4 = RC_PREV(slot); RC_ISSUE(js, tokn, s4); }
;                 bf16x8v At[4], Bv[2];
;                 const LAS unsigned char* sv = lds + RC_RG + slot * 16384;
; #pragma unroll
;                 for (int m = 0; m < 4; ++m) At[m] = *(const LAS bf16x8v*)(lds + RC_ST + js * 8192 + aoff + m * 1024);
; #pragma unroll
;                 for (int n = 0; n < 2; ++n) Bv[n] = *(const LAS bf16x8v*)(sv + boff + n * 1024);
;                 RC_WAITL();
; #pragma unroll
;                 for (int m = 0; m < 4; ++m)
; #pragma unroll
;                     for (int n = 0; n < 2; ++n) accY[m][n] = RC_MFMA(Bv[n], At[m], accY[m][n]);
;                 slot = RC_NEXT(slot);
;             }
	v_lshl_add_u64 v[108:109], v[218:219], 0, s[40:41]
	s_mov_b32 m0, s7
	v_lshl_add_u64 v[110:111], v[108:109], 0, s[62:63]
	global_load_lds_dwordx4 v[108:109], off
	s_add_i32 m0, s7, 0x2000
	v_add_u32_e32 v144, 0, v242
	global_load_lds_dwordx4 v[110:111], off
	v_add_u32_e32 v110, s1, v251
	s_add_i32 s1, s0, 1
	s_cmp_lg_u32 s0, 4
	s_cselect_b32 s0, s1, 0
	v_pk_mul_f32 v[98:99], v[98:99], v[116:117] op_sel_hi:[1,0]
	v_pk_mul_f32 v[96:97], v[96:97], v[116:117] op_sel_hi:[1,0]
	ds_read_b128 v[116:119], v144
	ds_read_b128 v[124:127], v144 offset:1024
	ds_read_b128 v[128:131], v144 offset:2048
	ds_read_b128 v[132:135], v144 offset:3072
	ds_read_b128 v[136:139], v110
	ds_read_b128 v[140:143], v110 offset:1024
	s_lshl_b32 s1, s0, 14
	s_add_i32 s7, s1, 0xc000
	s_cmp_lg_u32 s0, 0
	s_waitcnt lgkmcnt(0)
	s_cselect_b32 s7, s7, 0x20000
	s_waitcnt vmcnt(8)
	s_add_i32 s7, s45, s7
	s_waitcnt lgkmcnt(0)
	v_mfma_f32_16x16x32_bf16 v[110:113], v[140:143], v[128:131], v[112:115]
	s_barrier
	s_mov_b32 m0, s7
	v_mfma_f32_16x16x32_bf16 v[68:71], v[136:139], v[116:119], v[68:71]
	v_lshl_add_u64 v[114:115], v[108:109], 0, 64
	global_load_lds_dwordx4 v[114:115], off
	v_lshl_add_u64 v[114:115], v[108:109], 0, s[72:73]
	s_add_i32 m0, s7, 0x2000
	v_mfma_f32_16x16x32_bf16 v[72:75], v[140:143], v[116:119], v[72:75]
	global_load_lds_dwordx4 v[114:115], off
	v_add_u32_e32 v114, s1, v251
	s_add_i32 s1, s0, 1
	s_cmp_lg_u32 s0, 4
	s_cselect_b32 s0, s1, 0
	s_lshl_b32 s1, s0, 14
	v_mfma_f32_16x16x32_bf16 v[100:103], v[136:139], v[124:127], v[100:103]
	s_add_i32 s7, s1, 0xc000
	s_cmp_lg_u32 s0, 0
	s_cselect_b32 s7, s7, 0x20000
	v_mfma_f32_16x16x32_bf16 v[104:107], v[140:143], v[124:127], v[104:107]
	s_add_i32 s7, s45, s7
	s_mov_b32 m0, s7
	v_mfma_f32_16x16x32_bf16 v[116:119], v[136:139], v[128:131], v[120:123]
	v_mfma_f32_16x16x32_bf16 v[96:99], v[136:139], v[132:135], v[96:99]
	v_mfma_f32_16x16x32_bf16 v[92:95], v[140:143], v[132:135], v[92:95]
	s_nop 0
	ds_read_b128 v[120:123], v144 offset:8192
	ds_read_b128 v[124:127], v144 offset:9216
	ds_read_b128 v[128:131], v144 offset:10240
	ds_read_b128 v[132:135], v144 offset:11264
	ds_read_b128 v[136:139], v114
	ds_read_b128 v[140:143], v114 offset:1024
	s_waitcnt lgkmcnt(0)
	s_waitcnt vmcnt(9)
	s_waitcnt lgkmcnt(0)
	v_mfma_f32_16x16x32_bf16 v[114:117], v[136:139], v[128:131], v[116:119]
	s_barrier
	v_mfma_f32_16x16x32_bf16 v[68:71], v[136:139], v[120:123], v[68:71]
	s_nop 0
	v_lshl_add_u64 v[118:119], v[108:109], 0, s[66:67]
	global_load_lds_dwordx4 v[118:119], off
	v_mfma_f32_16x16x32_bf16 v[100:103], v[136:139], v[124:127], v[100:103]
	s_add_i32 m0, s7, 0x2000
	v_lshl_add_u64 v[118:119], v[108:109], 0, s[84:85]
	global_load_lds_dwordx4 v[118:119], off
	v_mfma_f32_16x16x32_bf16 v[96:99], v[136:139], v[132:135], v[96:99]
	v_add_u32_e32 v138, s1, v251
	s_add_i32 s1, s0, 1
	s_cmp_lg_u32 s0, 4
	s_cselect_b32 s7, s1, 0
	v_mfma_f32_16x16x32_bf16 v[72:75], v[140:143], v[120:123], v[72:75]
	s_lshl_b32 s0, s7, 14
	s_add_i32 s1, s0, 0xc000
	s_cmp_lg_u32 s7, 0
	v_mfma_f32_16x16x32_bf16 v[104:107], v[140:143], v[124:127], v[104:107]
	s_cselect_b32 s1, s1, 0x20000
	s_add_i32 s1, s45, s1
	s_mov_b32 m0, s1
	v_mfma_f32_16x16x32_bf16 v[110:113], v[140:143], v[128:131], v[110:113]
	v_mfma_f32_16x16x32_bf16 v[92:95], v[140:143], v[132:135], v[92:95]
	ds_read_b128 v[118:121], v144 offset:16384
	ds_read_b128 v[122:125], v144 offset:17408
	ds_read_b128 v[126:129], v144 offset:18432
	ds_read_b128 v[130:133], v144 offset:19456
	ds_read_b128 v[134:137], v138
	ds_read_b128 v[138:141], v138 offset:1024
	s_waitcnt lgkmcnt(0)
	s_waitcnt vmcnt(10)
	s_waitcnt lgkmcnt(0)
	v_mfma_f32_16x16x32_bf16 v[114:117], v[134:137], v[126:129], v[114:117]
	s_barrier
	v_mfma_f32_16x16x32_bf16 v[110:113], v[138:141], v[126:129], v[110:113]
	v_mfma_f32_16x16x32_bf16 v[126:129], v[138:141], v[130:133], v[92:95]
	s_nop 2
	v_lshl_add_u64 v[92:93], v[108:109], 0, s[16:17]
	global_load_lds_dwordx4 v[92:93], off
	v_lshl_add_u64 v[92:93], v[108:109], 0, s[18:19]
	s_add_i32 m0, s1, 0x2000
	v_mfma_f32_16x16x32_bf16 v[68:71], v[134:137], v[118:121], v[68:71]
	global_load_lds_dwordx4 v[92:93], off
	v_mfma_f32_16x16x32_bf16 v[72:75], v[138:141], v[118:121], v[72:75]
	v_mfma_f32_16x16x32_bf16 v[118:121], v[138:141], v[122:125], v[104:107]
	s_nop 2
	v_add_u32_e32 v104, s0, v251
	v_mfma_f32_16x16x32_bf16 v[100:103], v[134:137], v[122:125], v[100:103]
	s_add_u32 s0, s60, s53
	s_addc_u32 s1, s93, 0
	v_lshl_add_u64 v[108:109], s[0:1], 0, v[228:229]
	v_mfma_f32_16x16x32_bf16 v[122:125], v[134:137], v[130:133], v[96:99]
	ds_read_b128 v[92:95], v144 offset:24576
	s_nop 1
	ds_read_b128 v[96:99], v144 offset:25600
	ds_read_b128 v[130:133], v144 offset:26624
	ds_read_b128 v[134:137], v144 offset:27648
	ds_read_b128 v[138:141], v104
	ds_read_b128 v[142:145], v104 offset:1024
	s_waitcnt lgkmcnt(0)
	s_waitcnt lgkmcnt(0)
; template <int O> __device__ __forceinline__ float swz_xor(float v) { return __builtin_bit_cast(float, __builtin_amdgcn_ds_swizzle(__builtin_bit_cast(int, v), (O << 10) | 0x1f)); }
; __device__ __forceinline__ float get_xor32(float v, int lane) { return __builtin_bit_cast(float, __builtin_amdgcn_ds_bpermute((lane ^ 32) << 2, __builtin_bit_cast(int, v))); }
; __device__ __forceinline__ unsigned cvtpk(float lo, float hi) { f32x2_t v = {lo, hi}; bf16x2_t b = __builtin_convertvector(v, bf16x2_t); return __builtin_bit_cast(unsigned, b); }
; #define RC_MFMA(b, a, c) __builtin_amdgcn_mfma_f32_16x16x32_bf16((b), (a), (c), 0, 0, 0)
; template <int VAR  >
; __device__ __forceinline__ void ret_core_mfma(const bf16* P, const bf16* VT, const float* decay_logit  , bf16* YF, bf16* YB, float* PT, LAS unsigned char* lds, const int tid, const int bid, const int G) {
;     ...
;                 for (int m = 0; m < 4; ++m)
; #pragma unroll
;                     for (int n = 0; n < 2; ++n) accY[m][n] = RC_MFMA(Bv[n], At[m], accY[m][n]);
;                 slot = RC_NEXT(slot);
;             }
; #pragma unroll
;             for (int m = 0; m < 4; ++m) { v4u pw; pw.x = cvtpk(accY[m][0][0], accY[m][0][1]); pw.y = cvtpk(accY[m][0][2], accY[m][0][3]); pw.z = cvtpk(accY[m][1][0], accY[m][1][1]); pw.w = cvtpk(accY[m][1][2], accY[m][1][3]);
;                 *(v4u*)(Y + (rowbase + tok0 + 64 * wr + 16 * m + frc + zo) * DV + h * DVR + es * 128 + 32 * wc + 8 * fqc) = pw; }
; #pragma unroll
;             for (int m = 0; m < 4; ++m) { float sv = 0.f, sq = 0.f;
; #pragma unroll
;                 for (int n = 0; n < 2; ++n)
; #pragma unroll
;                     for (int ii = 0; ii < 4; ++ii) { const float yv = accY[m][n][ii]; sv += yv; sq += yv * yv; }
;                 sv += swz_xor<16>(sv); sq += swz_xor<16>(sq); sv += get_xor32(sv, lc); sq += get_xor32(sq, lc);
;                 float* sp = PT + (((size_t)((h * 2 + dir) * 16 + es * 4 + wc)) * M + (rowbase + tok0 + 64 * wr + 16 * m + frc + zo)) * 2;
;                 if (fqc == 0) *(f32x2_t*)sp = (f32x2_t){sv, sq}; }
	v_mfma_f32_16x16x32_bf16 v[146:149], v[138:141], v[92:95], v[68:71]
	s_mov_b32 s0, 0x30000
	v_mfma_f32_16x16x32_bf16 v[150:153], v[142:145], v[92:95], v[72:75]
	v_mfma_f32_16x16x32_bf16 v[104:107], v[138:141], v[96:99], v[100:103]
	v_mfma_f32_16x16x32_bf16 v[100:103], v[142:145], v[96:99], v[118:121]
	v_mfma_f32_16x16x32_bf16 v[92:95], v[142:145], v[130:133], v[110:113]
	s_nop 2
	v_lshl_add_u64 v[112:113], v[108:109], 0, v[2:3]
	v_mfma_f32_16x16x32_bf16 v[96:99], v[138:141], v[130:133], v[114:117]
	v_lshlrev_b64 v[112:113], 12, v[112:113]
	v_cvt_pk_bf16_f32 v108, v146, v147
	v_cvt_pk_bf16_f32 v109, v148, v149
	v_lshl_add_u64 v[114:115], v[226:227], 1, s[54:55]
	v_lshl_add_u64 v[112:113], v[114:115], 0, v[112:113]
	v_cvt_pk_bf16_f32 v110, v150, v151
	v_cvt_pk_bf16_f32 v111, v152, v153
	v_add_co_u32_e32 v114, vcc, s58, v112
	v_mfma_f32_16x16x32_bf16 v[72:75], v[138:141], v[134:137], v[122:125]
	global_store_dwordx4 v[112:113], v[108:111], off
	v_addc_co_u32_e32 v115, vcc, 0, v113, vcc
	v_mfma_f32_16x16x32_bf16 v[68:71], v[142:145], v[134:137], v[126:129]
	v_cvt_pk_bf16_f32 v108, v104, v105
	v_cvt_pk_bf16_f32 v109, v106, v107
	v_cvt_pk_bf16_f32 v110, v100, v101
	v_cvt_pk_bf16_f32 v111, v102, v103
	global_store_dwordx4 v[114:115], v[108:111], off
	v_add_co_u32_e32 v114, vcc, s59, v112
	s_nop 0
	v_cvt_pk_bf16_f32 v108, v96, v97
	v_addc_co_u32_e32 v115, vcc, 0, v113, vcc
	v_cvt_pk_bf16_f32 v109, v98, v99
	v_cvt_pk_bf16_f32 v110, v92, v93
	v_cvt_pk_bf16_f32 v111, v94, v95
	v_add_co_u32_e32 v112, vcc, s0, v112
	global_store_dwordx4 v[114:115], v[108:111], off
	s_nop 0
	v_addc_co_u32_e32 v113, vcc, 0, v113, vcc
	v_cvt_pk_bf16_f32 v108, v72, v73
	v_cvt_pk_bf16_f32 v109, v74, v75
	v_cvt_pk_bf16_f32 v110, v68, v69
	v_cvt_pk_bf16_f32 v111, v70, v71
	global_store_dwordx4 v[112:113], v[108:111], off
	v_pk_mul_f32 v[112:113], v[146:147], v[146:147]
	v_pk_mul_f32 v[116:117], v[150:151], v[150:151]
	v_add_f32_e32 v110, 0, v146
	v_add_f32_e32 v110, v147, v110
	v_add_f32_e32 v115, v148, v110
	v_pk_mul_f32 v[110:111], v[148:149], v[148:149]
	v_fmac_f32_e32 v113, v146, v146
	v_add_f32_e32 v112, v110, v113
	v_add_f32_e32 v110, v149, v115
	v_mov_b32_e32 v148, v150
	v_add_f32_e32 v113, v150, v110
	v_pk_mul_f32 v[110:111], v[148:149], v[148:149]
	v_lshlrev_b32_e32 v108, 2, v230
	v_add_f32_e32 v111, v111, v112
	v_add_f32_e32 v111, v110, v111
	v_add_f32_e32 v110, v151, v113
	v_pk_mul_f32 v[112:113], v[152:153], v[152:153]
	v_add_f32_e32 v111, v117, v111
	v_add_f32_e32 v110, v152, v110
	v_add_f32_e32 v113, v112, v111
	v_mul_f32_e32 v111, v153, v153
	v_mov_b32_e32 v112, v153
	v_pk_add_f32 v[110:111], v[112:113], v[110:111]
	v_mov_b32_e32 v112, v110
	v_mov_b32_e32 v113, v111
	s_nop 1
	v_permlane16_swap_b32_e32 v112, v110
	v_permlane16_swap_b32_e32 v113, v111
	v_xor_b32_e32 v114, 0x80, v108
	v_lshl_add_u64 v[108:109], s[78:79], 0, v[230:231]
	v_lshl_add_u64 v[108:109], v[108:109], 0, v[228:229]
	v_lshl_add_u64 v[108:109], v[108:109], 0, s[60:61]
	s_waitcnt lgkmcnt(0)
	v_pk_add_f32 v[110:111], v[110:111], v[112:113]
	v_mov_b32_e32 v112, v110
	v_mov_b32_e32 v113, v111
	s_nop 1
	v_permlane32_swap_b32_e32 v112, v110
	v_permlane32_swap_b32_e32 v113, v111
	v_cmp_gt_u32_e32 vcc, 16, v230
	v_lshl_add_u64 v[108:109], v[108:109], 3, s[14:15]
	s_and_saveexec_b64 s[0:1], vcc
	s_cbranch_execz .LBB0_57
	s_waitcnt lgkmcnt(0)
	v_pk_add_f32 v[110:111], v[110:111], v[112:113]
	global_store_dwordx2 v[108:109], v[110:111], off
; template <int O> __device__ __forceinline__ float swz_xor(float v) { return __builtin_bit_cast(float, __builtin_amdgcn_ds_swizzle(__builtin_bit_cast(int, v), (O << 10) | 0x1f)); }
; __device__ __forceinline__ float get_xor32(float v, int lane) { return __builtin_bit_cast(float, __builtin_amdgcn_ds_bpermute((lane ^ 32) << 2, __builtin_bit_cast(int, v))); }
; template <int VAR  >
; __device__ __forceinline__ void ret_core_mfma(const bf16* P, const bf16* VT, const float* decay_logit  , bf16* YF, bf16* YB, float* PT, LAS unsigned char* lds, const int tid, const int bid, const int G) {
;     ...
;             for (int m = 0; m < 4; ++m) { float sv = 0.f, sq = 0.f;
; #pragma unroll
;                 for (int n = 0; n < 2; ++n)
; #pragma unroll
;                     for (int ii = 0; ii < 4; ++ii) { const float yv = accY[m][n][ii]; sv += yv; sq += yv * yv; }
;                 sv += swz_xor<16>(sv); sq += swz_xor<16>(sq); sv += get_xor32(sv, lc); sq += get_xor32(sq, lc);
;                 float* sp = PT + (((size_t)((h * 2 + dir) * 16 + es * 4 + wc)) * M + (rowbase + tok0 + 64 * wr + 16 * m + frc + zo)) * 2;
;                 if (fqc == 0) *(f32x2_t*)sp = (f32x2_t){sv, sq}; }
.LBB0_57:
	s_or_b64 exec, exec, s[0:1]
	v_add_f32_e32 v110, 0, v104
	v_add_f32_e32 v110, v105, v110
	v_add_f32_e32 v115, v106, v110
	s_waitcnt lgkmcnt(0)
	v_pk_mul_f32 v[112:113], v[104:105], v[104:105]
	v_pk_mul_f32 v[110:111], v[106:107], v[106:107]
	v_fmac_f32_e32 v113, v104, v104
	v_add_f32_e32 v104, v107, v115
	v_mov_b32_e32 v106, v100
	v_add_f32_e32 v110, v110, v113
	v_add_f32_e32 v111, v100, v104
	v_pk_mul_f32 v[104:105], v[106:107], v[106:107]
	v_pk_mul_f32 v[106:107], v[102:103], v[102:103]
	v_add_f32_e32 v105, v105, v110
	v_add_f32_e32 v105, v104, v105
	v_add_f32_e32 v104, v101, v111
	v_pk_mul_f32 v[100:101], v[100:101], v[100:101]
	v_add_f32_e32 v104, v102, v104
	v_add_f32_e32 v100, v101, v105
	v_add_f32_e32 v101, v106, v100
	v_mul_f32_e32 v105, v103, v103
	v_mov_b32_e32 v100, v103
	v_pk_add_f32 v[100:101], v[100:101], v[104:105]
	v_mov_b32_e32 v102, v100
	v_mov_b32_e32 v103, v101
	s_nop 1
	v_permlane16_swap_b32_e32 v102, v100
	v_permlane16_swap_b32_e32 v103, v101
	s_waitcnt lgkmcnt(0)
	v_pk_add_f32 v[100:101], v[100:101], v[102:103]
	v_mov_b32_e32 v102, v100
	v_mov_b32_e32 v103, v101
	s_nop 1
	v_permlane32_swap_b32_e32 v102, v100
	v_permlane32_swap_b32_e32 v103, v101
	s_and_saveexec_b64 s[0:1], vcc
	s_cbranch_execz .LBB0_59
	s_waitcnt lgkmcnt(0)
	v_pk_add_f32 v[100:101], v[100:101], v[102:103]
	global_store_dwordx2 v[108:109], v[100:101], off offset:128
.LBB0_59:
	s_or_b64 exec, exec, s[0:1]
	v_add_f32_e32 v100, 0, v96
	v_add_f32_e32 v100, v97, v100
	v_add_f32_e32 v104, v98, v100
	s_waitcnt lgkmcnt(0)
	v_pk_mul_f32 v[102:103], v[96:97], v[96:97]
	v_pk_mul_f32 v[100:101], v[98:99], v[98:99]
	v_fmac_f32_e32 v103, v96, v96
	v_add_f32_e32 v96, v99, v104
	v_mov_b32_e32 v98, v92
	v_add_f32_e32 v100, v100, v103
	v_add_f32_e32 v101, v92, v96
	v_pk_mul_f32 v[96:97], v[98:99], v[98:99]
	v_pk_mul_f32 v[98:99], v[94:95], v[94:95]
	v_add_f32_e32 v97, v97, v100
	v_add_f32_e32 v97, v96, v97
	v_add_f32_e32 v96, v93, v101
	v_pk_mul_f32 v[92:93], v[92:93], v[92:93]
	v_add_f32_e32 v96, v94, v96
	v_add_f32_e32 v92, v93, v97
	v_add_f32_e32 v93, v98, v92
	v_mul_f32_e32 v97, v95, v95
	v_mov_b32_e32 v92, v95
	v_pk_add_f32 v[92:93], v[92:93], v[96:97]
	v_mov_b32_e32 v94, v92
	v_mov_b32_e32 v95, v93
	s_nop 1
	v_permlane16_swap_b32_e32 v94, v92
	v_permlane16_swap_b32_e32 v95, v93
	s_waitcnt lgkmcnt(0)
	v_pk_add_f32 v[92:93], v[92:93], v[94:95]
	v_mov_b32_e32 v94, v92
	v_mov_b32_e32 v95, v93
	s_nop 1
	v_permlane32_swap_b32_e32 v94, v92
	v_permlane32_swap_b32_e32 v95, v93
	s_and_saveexec_b64 s[0:1], vcc
	s_cbranch_execz .LBB0_61
	s_waitcnt lgkmcnt(0)
	v_pk_add_f32 v[92:93], v[92:93], v[94:95]
	global_store_dwordx2 v[108:109], v[92:93], off offset:256
.LBB0_61:
	s_or_b64 exec, exec, s[0:1]
	v_add_f32_e32 v92, 0, v72
	v_add_f32_e32 v92, v73, v92
	v_add_f32_e32 v96, v74, v92
	s_waitcnt lgkmcnt(0)
	v_pk_mul_f32 v[94:95], v[72:73], v[72:73]
	v_pk_mul_f32 v[92:93], v[74:75], v[74:75]
	v_fmac_f32_e32 v95, v72, v72
	v_add_f32_e32 v72, v75, v96
	v_mov_b32_e32 v74, v68
	v_add_f32_e32 v92, v92, v95
	v_add_f32_e32 v93, v68, v72
	v_pk_mul_f32 v[72:73], v[74:75], v[74:75]
	v_pk_mul_f32 v[74:75], v[70:71], v[70:71]
	v_add_f32_e32 v73, v73, v92
	v_add_f32_e32 v73, v72, v73
	v_add_f32_e32 v72, v69, v93
	v_pk_mul_f32 v[68:69], v[68:69], v[68:69]
	v_add_f32_e32 v72, v70, v72
	v_add_f32_e32 v68, v69, v73
	v_add_f32_e32 v69, v74, v68
	v_mul_f32_e32 v73, v71, v71
	v_mov_b32_e32 v68, v71
	v_pk_add_f32 v[68:69], v[68:69], v[72:73]
	v_mov_b32_e32 v70, v68
	v_mov_b32_e32 v71, v69
	s_nop 1
	v_permlane16_swap_b32_e32 v70, v68
	v_permlane16_swap_b32_e32 v71, v69
	s_waitcnt lgkmcnt(0)
	v_pk_add_f32 v[68:69], v[68:69], v[70:71]
	v_mov_b32_e32 v70, v68
	v_mov_b32_e32 v71, v69
	s_nop 1
	v_permlane32_swap_b32_e32 v70, v68
	v_permlane32_swap_b32_e32 v71, v69
	s_and_saveexec_b64 s[0:1], vcc
	s_cbranch_execz .LBB0_42
	s_waitcnt lgkmcnt(0)
	v_pk_add_f32 v[68:69], v[68:69], v[70:71]
	global_store_dwordx2 v[108:109], v[68:69], off offset:384
	s_branch .LBB0_42

; __device__ __forceinline__ float epi_xor16(float v) { return __builtin_bit_cast(float, __builtin_amdgcn_ds_swizzle(__builtin_bit_cast(int, v), (16 << 10) | 0x1f)); }
; __device__ __forceinline__ float epi_xor32(float v, int lane) { return __builtin_bit_cast(float, __builtin_amdgcn_ds_bpermute((lane ^ 32) << 2, __builtin_bit_cast(int, v))); }
;     __device__ __forceinline__ void operator()(const f32x4 (&acc)[2][2][4][2], const Unit& u, int wr, int wc, int fr, int fq) const {
;     ...
;         u32x4 xa[4][2];
; #pragma unroll
;         for (int m = 0; m < 4; ++m)
; #pragma unroll
;             for (int bj = 0; bj < 2; ++bj) xa[m][bj] = *(const u32x4*)(XB + (size_t)(row0 + m * 16) * 1024 + col0 + bj * HALF);
;         float gp[2][8];
; #pragma unroll
;         for (int bj = 0; bj < 2; ++bj) { const f32x4 a = *(const f32x4*)(gpost + col0 + bj * HALF), b = *(const f32x4*)(gpost + col0 + bj * HALF + 4);
;             gp[bj][0] = a[0]; gp[bj][1] = a[1]; gp[bj][2] = a[2]; gp[bj][3] = a[3]; gp[bj][4] = b[0]; gp[bj][5] = b[1]; gp[bj][6] = b[2]; gp[bj][7] = b[3]; }
; #pragma unroll
;         for (int ai = 0; ai < 2; ++ai)
; #pragma unroll
;             for (int m = 0; m < 4; ++m) { f32x2 s2v = {0.f, 0.f};
; #pragma unroll
;                 for (int bj = 0; bj < 2; ++bj)
; #pragma unroll
;                     for (int n = 0; n < 2; ++n) { const f32x2 a0 = {acc[ai][bj][m][n][0], acc[ai][bj][m][n][1]}, a1 = {acc[ai][bj][m][n][2], acc[ai][bj][m][n][3]}; s2v += a0 * a0; s2v += a1 * a1; }
;                 float s = s2v[0] + s2v[1];
;                 s += epi_xor16(s); s += epi_xor32(s, lane);
;                 if (fq == 0) scr[wc * 256 + ai * HALF + wr * 64 + m * 16 + fr] = s; }
.LBB0_581:
	s_lshl_b32 s8, s13, 8
	v_add_u32_e32 v196, s8, v229
	v_lshl_or_b32 v192, s12, 8, v231
	v_ashrrev_i32_e32 v193, 31, v192
	v_ashrrev_i32_e32 v197, 31, v196
	v_or_b32_e32 v222, 16, v196
	v_lshl_add_u64 v[198:199], v[192:193], 1, s[54:55]
	v_lshlrev_b64 v[224:225], 11, v[196:197]
	v_ashrrev_i32_e32 v223, 31, v222
	v_or_b32_e32 v218, 32, v196
	v_lshl_add_u64 v[60:61], v[198:199], 0, v[224:225]
	v_lshlrev_b64 v[220:221], 11, v[222:223]
	v_ashrrev_i32_e32 v219, 31, v218
	v_or_b32_e32 v214, 48, v196
	global_load_dwordx4 v[176:179], v[60:61], off
	global_load_dwordx4 v[172:175], v[60:61], off offset:256
	v_lshl_add_u64 v[60:61], v[198:199], 0, v[220:221]
	v_lshlrev_b64 v[216:217], 11, v[218:219]
	v_ashrrev_i32_e32 v215, 31, v214
	global_load_dwordx4 v[168:171], v[60:61], off
	global_load_dwordx4 v[164:167], v[60:61], off offset:256
	v_lshl_add_u64 v[60:61], v[198:199], 0, v[216:217]
	v_lshlrev_b64 v[212:213], 11, v[214:215]
	global_load_dwordx4 v[160:163], v[60:61], off
	global_load_dwordx4 v[156:159], v[60:61], off offset:256
	v_lshl_add_u64 v[60:61], v[198:199], 0, v[212:213]
	v_lshl_add_u64 v[68:69], v[192:193], 2, s[52:53]
	global_load_dwordx4 v[152:155], v[60:61], off
	global_load_dwordx4 v[148:151], v[60:61], off offset:256
	global_load_dwordx4 v[76:79], v[68:69], off offset:16
	global_load_dwordx4 v[80:83], v[68:69], off
	s_nop 0
	global_load_dwordx4 v[60:63], v[68:69], off offset:528
	s_nop 0
	global_load_dwordx4 v[68:71], v[68:69], off offset:512
	v_pk_mul_f32 v[194:195], v[146:147], v[146:147]
	s_nop 0
	v_pk_fma_f32 v[194:195], v[144:145], v[144:145], v[194:195]
	s_nop 0
	v_pk_fma_f32 v[194:195], v[140:141], v[140:141], v[194:195]
	s_nop 0
	v_pk_fma_f32 v[194:195], v[142:143], v[142:143], v[194:195]
	s_nop 0
	v_pk_fma_f32 v[194:195], v[136:137], v[136:137], v[194:195]
	s_nop 0
	v_pk_fma_f32 v[194:195], v[138:139], v[138:139], v[194:195]
	s_nop 0
	v_pk_fma_f32 v[194:195], v[132:133], v[132:133], v[194:195]
	s_nop 0
	v_pk_fma_f32 v[194:195], v[134:135], v[134:135], v[194:195]
	s_nop 0
	v_add_f32_e32 v194, v194, v195
	v_mov_b32_e32 v195, v194
	s_nop 1
	v_permlane16_swap_b32_e32 v195, v194
	s_waitcnt lgkmcnt(0)
	v_add_f32_e32 v194, v194, v195
	v_mov_b32_e32 v195, v194
	s_nop 1
	v_permlane32_swap_b32_e32 v195, v194
	s_and_saveexec_b64 s[0:1], s[2:3]
	s_cbranch_execz .LBB0_583
	s_waitcnt lgkmcnt(0)
	v_add_f32_e32 v194, v194, v195
	ds_write_b32 v241, v194
.LBB0_583:
	s_or_b64 exec, exec, s[0:1]
	s_waitcnt lgkmcnt(0)
	v_pk_mul_f32 v[194:195], v[130:131], v[130:131]
	s_nop 0
	v_pk_fma_f32 v[194:195], v[128:129], v[128:129], v[194:195]
	s_nop 0
	v_pk_fma_f32 v[194:195], v[124:125], v[124:125], v[194:195]
	s_nop 0
	v_pk_fma_f32 v[194:195], v[126:127], v[126:127], v[194:195]
	s_nop 0
	v_pk_fma_f32 v[194:195], v[120:121], v[120:121], v[194:195]
	s_nop 0
	v_pk_fma_f32 v[194:195], v[122:123], v[122:123], v[194:195]
	s_nop 0
	v_pk_fma_f32 v[194:195], v[116:117], v[116:117], v[194:195]
	s_nop 0
	v_pk_fma_f32 v[194:195], v[118:119], v[118:119], v[194:195]
	s_nop 0
	v_add_f32_e32 v194, v194, v195
	v_mov_b32_e32 v195, v194
	s_nop 1
	v_permlane16_swap_b32_e32 v195, v194
	s_waitcnt lgkmcnt(0)
	v_add_f32_e32 v194, v194, v195
	v_mov_b32_e32 v195, v194
	s_nop 1
	v_permlane32_swap_b32_e32 v195, v194
	s_and_saveexec_b64 s[0:1], s[2:3]
	s_cbranch_execz .LBB0_585
	s_waitcnt lgkmcnt(0)
	v_add_f32_e32 v194, v194, v195
	ds_write_b32 v241, v194 offset:64
.LBB0_585:
	s_or_b64 exec, exec, s[0:1]
	s_waitcnt lgkmcnt(0)
	v_pk_mul_f32 v[194:195], v[114:115], v[114:115]
	s_nop 0
	v_pk_fma_f32 v[194:195], v[112:113], v[112:113], v[194:195]
	s_nop 0
	v_pk_fma_f32 v[194:195], v[108:109], v[108:109], v[194:195]
	s_nop 0
	v_pk_fma_f32 v[194:195], v[110:111], v[110:111], v[194:195]
	s_nop 0
	v_pk_fma_f32 v[194:195], v[104:105], v[104:105], v[194:195]
	s_nop 0
	v_pk_fma_f32 v[194:195], v[106:107], v[106:107], v[194:195]
	s_nop 0
	v_pk_fma_f32 v[194:195], v[100:101], v[100:101], v[194:195]
	s_nop 0
	v_pk_fma_f32 v[194:195], v[102:103], v[102:103], v[194:195]
	s_nop 0
	v_add_f32_e32 v194, v194, v195
	v_mov_b32_e32 v195, v194
	s_nop 1
	v_permlane16_swap_b32_e32 v195, v194
	s_waitcnt lgkmcnt(0)
	v_add_f32_e32 v194, v194, v195
	v_mov_b32_e32 v195, v194
	s_nop 1
	v_permlane32_swap_b32_e32 v195, v194
	s_and_saveexec_b64 s[0:1], s[2:3]
	s_cbranch_execz .LBB0_587
	s_waitcnt lgkmcnt(0)
	v_add_f32_e32 v194, v194, v195
	ds_write_b32 v241, v194 offset:128
; __device__ __forceinline__ float epi_xor16(float v) { return __builtin_bit_cast(float, __builtin_amdgcn_ds_swizzle(__builtin_bit_cast(int, v), (16 << 10) | 0x1f)); }
; __device__ __forceinline__ float epi_xor32(float v, int lane) { return __builtin_bit_cast(float, __builtin_amdgcn_ds_bpermute((lane ^ 32) << 2, __builtin_bit_cast(int, v))); }
;     __device__ __forceinline__ void operator()(const f32x4 (&acc)[2][2][4][2], const Unit& u, int wr, int wc, int fr, int fq) const {
;     ...
;             for (int m = 0; m < 4; ++m) { f32x2 s2v = {0.f, 0.f};
; #pragma unroll
;                 for (int bj = 0; bj < 2; ++bj)
; #pragma unroll
;                     for (int n = 0; n < 2; ++n) { const f32x2 a0 = {acc[ai][bj][m][n][0], acc[ai][bj][m][n][1]}, a1 = {acc[ai][bj][m][n][2], acc[ai][bj][m][n][3]}; s2v += a0 * a0; s2v += a1 * a1; }
;                 float s = s2v[0] + s2v[1];
;                 s += epi_xor16(s); s += epi_xor32(s, lane);
;                 if (fq == 0) scr[wc * 256 + ai * HALF + wr * 64 + m * 16 + fr] = s; }
.LBB0_587:
	s_or_b64 exec, exec, s[0:1]
	s_waitcnt lgkmcnt(0)
	v_pk_mul_f32 v[194:195], v[98:99], v[98:99]
	s_nop 0
	v_pk_fma_f32 v[194:195], v[96:97], v[96:97], v[194:195]
	s_nop 0
	v_pk_fma_f32 v[194:195], v[92:93], v[92:93], v[194:195]
	s_nop 0
	v_pk_fma_f32 v[194:195], v[94:95], v[94:95], v[194:195]
	s_nop 0
	v_pk_fma_f32 v[194:195], v[88:89], v[88:89], v[194:195]
	s_nop 0
	v_pk_fma_f32 v[194:195], v[90:91], v[90:91], v[194:195]
	s_nop 0
	v_pk_fma_f32 v[194:195], v[84:85], v[84:85], v[194:195]
	s_nop 0
	v_pk_fma_f32 v[194:195], v[86:87], v[86:87], v[194:195]
	s_nop 0
	v_add_f32_e32 v194, v194, v195
	v_mov_b32_e32 v195, v194
	s_nop 1
	v_permlane16_swap_b32_e32 v195, v194
	s_waitcnt lgkmcnt(0)
	v_add_f32_e32 v194, v194, v195
	v_mov_b32_e32 v195, v194
	s_nop 1
	v_permlane32_swap_b32_e32 v195, v194
	s_and_saveexec_b64 s[0:1], s[2:3]
	s_cbranch_execz .LBB0_589
	s_waitcnt lgkmcnt(0)
	v_add_f32_e32 v194, v194, v195
	ds_write_b32 v241, v194 offset:192
.LBB0_589:
	s_or_b64 exec, exec, s[0:1]
	s_waitcnt lgkmcnt(0)
	v_pk_mul_f32 v[194:195], v[74:75], v[74:75]
	s_nop 0
	v_pk_fma_f32 v[194:195], v[72:73], v[72:73], v[194:195]
	s_nop 0
	v_pk_fma_f32 v[194:195], v[64:65], v[64:65], v[194:195]
	s_nop 0
	v_pk_fma_f32 v[194:195], v[66:67], v[66:67], v[194:195]
	s_nop 0
	v_pk_fma_f32 v[194:195], v[56:57], v[56:57], v[194:195]
	s_nop 0
	v_pk_fma_f32 v[194:195], v[58:59], v[58:59], v[194:195]
	s_nop 0
	v_pk_fma_f32 v[194:195], v[52:53], v[52:53], v[194:195]
	s_nop 0
	v_pk_fma_f32 v[194:195], v[54:55], v[54:55], v[194:195]
	s_nop 0
	v_add_f32_e32 v194, v194, v195
	v_mov_b32_e32 v195, v194
	s_nop 1
	v_permlane16_swap_b32_e32 v195, v194
	s_waitcnt lgkmcnt(0)
	v_add_f32_e32 v194, v194, v195
	v_mov_b32_e32 v195, v194
	s_nop 1
	v_permlane32_swap_b32_e32 v195, v194
	s_and_saveexec_b64 s[0:1], s[2:3]
	s_cbranch_execz .LBB0_591
	s_waitcnt lgkmcnt(0)
	v_add_f32_e32 v194, v194, v195
	ds_write_b32 v241, v194 offset:512
.LBB0_591:
	s_or_b64 exec, exec, s[0:1]
	s_waitcnt lgkmcnt(0)
	v_pk_mul_f32 v[194:195], v[50:51], v[50:51]
	s_nop 0
	v_pk_fma_f32 v[194:195], v[48:49], v[48:49], v[194:195]
	s_nop 0
	v_pk_fma_f32 v[194:195], v[44:45], v[44:45], v[194:195]
	s_nop 0
	v_pk_fma_f32 v[194:195], v[46:47], v[46:47], v[194:195]
	s_nop 0
	v_pk_fma_f32 v[194:195], v[40:41], v[40:41], v[194:195]
	s_nop 0
	v_pk_fma_f32 v[194:195], v[42:43], v[42:43], v[194:195]
	s_nop 0
	v_pk_fma_f32 v[194:195], v[36:37], v[36:37], v[194:195]
	s_nop 0
	v_pk_fma_f32 v[194:195], v[38:39], v[38:39], v[194:195]
	s_nop 0
	v_add_f32_e32 v194, v194, v195
	v_mov_b32_e32 v195, v194
	s_nop 1
	v_permlane16_swap_b32_e32 v195, v194
	s_waitcnt lgkmcnt(0)
	v_add_f32_e32 v194, v194, v195
	v_mov_b32_e32 v195, v194
	s_nop 1
	v_permlane32_swap_b32_e32 v195, v194
	s_and_saveexec_b64 s[0:1], s[2:3]
	s_cbranch_execz .LBB0_593
	s_waitcnt lgkmcnt(0)
	v_add_f32_e32 v194, v194, v195
	ds_write_b32 v241, v194 offset:576
.LBB0_593:
	s_or_b64 exec, exec, s[0:1]
	s_waitcnt lgkmcnt(0)
	v_pk_mul_f32 v[194:195], v[34:35], v[34:35]
	s_nop 0
	v_pk_fma_f32 v[194:195], v[32:33], v[32:33], v[194:195]
	s_nop 0
	v_pk_fma_f32 v[194:195], v[28:29], v[28:29], v[194:195]
	s_nop 0
	v_pk_fma_f32 v[194:195], v[30:31], v[30:31], v[194:195]
	s_nop 0
	v_pk_fma_f32 v[194:195], v[24:25], v[24:25], v[194:195]
	s_nop 0
	v_pk_fma_f32 v[194:195], v[26:27], v[26:27], v[194:195]
	s_nop 0
	v_pk_fma_f32 v[194:195], v[20:21], v[20:21], v[194:195]
	s_nop 0
	v_pk_fma_f32 v[194:195], v[22:23], v[22:23], v[194:195]
	s_nop 0
	v_add_f32_e32 v194, v194, v195
	v_mov_b32_e32 v195, v194
	s_nop 1
	v_permlane16_swap_b32_e32 v195, v194
	s_waitcnt lgkmcnt(0)
	v_add_f32_e32 v194, v194, v195
	v_mov_b32_e32 v195, v194
	s_nop 1
	v_permlane32_swap_b32_e32 v195, v194
	s_and_saveexec_b64 s[0:1], s[2:3]
	s_cbranch_execz .LBB0_595
	s_waitcnt lgkmcnt(0)
	v_add_f32_e32 v194, v194, v195
	ds_write_b32 v241, v194 offset:640
.LBB0_595:
	s_or_b64 exec, exec, s[0:1]
	s_waitcnt lgkmcnt(0)
	v_pk_mul_f32 v[194:195], v[18:19], v[18:19]
	s_nop 0
	v_pk_fma_f32 v[194:195], v[16:17], v[16:17], v[194:195]
	s_nop 0
	v_pk_fma_f32 v[194:195], v[12:13], v[12:13], v[194:195]
	s_nop 0
	v_pk_fma_f32 v[194:195], v[14:15], v[14:15], v[194:195]
	s_nop 0
	v_pk_fma_f32 v[194:195], v[8:9], v[8:9], v[194:195]
	s_nop 0
	v_pk_fma_f32 v[194:195], v[10:11], v[10:11], v[194:195]
	s_nop 0
	v_pk_fma_f32 v[194:195], v[4:5], v[4:5], v[194:195]
	s_nop 0
	v_pk_fma_f32 v[194:195], v[6:7], v[6:7], v[194:195]
	s_nop 0
	v_add_f32_e32 v194, v194, v195
	v_mov_b32_e32 v195, v194
	s_nop 1
	v_permlane16_swap_b32_e32 v195, v194
	s_waitcnt lgkmcnt(0)
	v_add_f32_e32 v194, v194, v195
	v_mov_b32_e32 v195, v194
	s_nop 1
	v_permlane32_swap_b32_e32 v195, v194
	s_and_saveexec_b64 s[0:1], s[2:3]
	s_cbranch_execz .LBB0_597
	s_waitcnt lgkmcnt(0)
	v_add_f32_e32 v194, v194, v195
	ds_write_b32 v241, v194 offset:704

; __device__ __forceinline__ unsigned cvt_pk_bf16(float lo, float hi) { unsigned r; asm volatile("v_cvt_pk_bf16_f32 %0, %1, %2" : "=v"(r) : "v"(lo), "v"(hi)); return r; }
; __device__ __forceinline__ float epi_xor16(float v) { return __builtin_bit_cast(float, __builtin_amdgcn_ds_swizzle(__builtin_bit_cast(int, v), (16 << 10) | 0x1f)); }
; __device__ __forceinline__ float epi_xor32(float v, int lane) { return __builtin_bit_cast(float, __builtin_amdgcn_ds_bpermute((lane ^ 32) << 2, __builtin_bit_cast(int, v))); }
;     __device__ __forceinline__ void operator()(const f32x4 (&acc)[2][2][4][2], const Unit& u, int wr, int wc, int fr, int fq) const {
;     ...
;                         for (int e = 0; e < 4; e += 2) { const int q = n * 4 + e; const unsigned w = xw[q >> 1];
;                             const f32x2 xv = {__builtin_bit_cast(float, w << 16), __builtin_bit_cast(float, w & 0xffff0000u)}, av = {acc[ai][bj][m][n][e], acc[ai][bj][m][n][e + 1]}, gv = {gp[bj][q], gp[bj][q + 1]};
;                             const f32x2 ov = xv + av * (gv * rF); s2p += ov * ov; o[q] = ov[0]; o[q + 1] = ov[1]; }
;                     if (OUT) { float* op = OUT + (size_t)row * 1024 + col0 + bj * HALF;
;                         __builtin_nontemporal_store((f32x4){o[0], o[1], o[2], o[3]}, (f32x4*)op); __builtin_nontemporal_store((f32x4){o[4], o[5], o[6], o[7]}, (f32x4*)(op + 4)); }
;                     else { u32x4 w; w.x = cvt_pk_bf16(o[0], o[1]); w.y = cvt_pk_bf16(o[2], o[3]); w.z = cvt_pk_bf16(o[4], o[5]); w.w = cvt_pk_bf16(o[6], o[7]);
;                         *(u32x4*)(XB + (size_t)row * 1024 + col0 + bj * HALF) = w; } }
;                 float s2 = s2p[0] + s2p[1];
;                 s2 += epi_xor16(s2); s2 += epi_xor32(s2, lane);
;                 if (fq == 0) scr[wc * 256 + (row & 255)] = s2; }
.LBB0_618:
	v_pk_mul_f32 v[146:147], v[146:147], v[146:147]
	s_nop 0
	v_pk_fma_f32 v[144:145], v[144:145], v[144:145], v[146:147]
	s_nop 0
	v_pk_fma_f32 v[140:141], v[140:141], v[140:141], v[144:145]
	s_nop 0
	v_pk_fma_f32 v[140:141], v[142:143], v[142:143], v[140:141]
	s_nop 0
	v_pk_fma_f32 v[136:137], v[136:137], v[136:137], v[140:141]
	s_nop 0
	v_pk_fma_f32 v[136:137], v[138:139], v[138:139], v[136:137]
	s_nop 0
	v_pk_fma_f32 v[132:133], v[132:133], v[132:133], v[136:137]
	s_nop 0
	v_pk_fma_f32 v[132:133], v[134:135], v[134:135], v[132:133]
	s_nop 0
	v_add_f32_e32 v132, v132, v133
	v_mov_b32_e32 v133, v132
	s_nop 1
	v_permlane16_swap_b32_e32 v133, v132
	s_waitcnt lgkmcnt(0)
	v_add_f32_e32 v132, v132, v133
	v_mov_b32_e32 v133, v132
	s_nop 1
	v_permlane32_swap_b32_e32 v133, v132
	s_and_saveexec_b64 s[0:1], s[2:3]
	s_cbranch_execz .LBB0_620
	s_waitcnt lgkmcnt(0)
	v_add_f32_e32 v132, v132, v133
	ds_write_b32 v244, v132

; __device__ __forceinline__ unsigned cvt_pk_bf16(float lo, float hi) { unsigned r; asm volatile("v_cvt_pk_bf16_f32 %0, %1, %2" : "=v"(r) : "v"(lo), "v"(hi)); return r; }
; __device__ __forceinline__ float epi_xor16(float v) { return __builtin_bit_cast(float, __builtin_amdgcn_ds_swizzle(__builtin_bit_cast(int, v), (16 << 10) | 0x1f)); }
; __device__ __forceinline__ float epi_xor32(float v, int lane) { return __builtin_bit_cast(float, __builtin_amdgcn_ds_bpermute((lane ^ 32) << 2, __builtin_bit_cast(int, v))); }
;     __device__ __forceinline__ void operator()(const f32x4 (&acc)[2][2][4][2], const Unit& u, int wr, int wc, int fr, int fq) const {
;     ...
;                         for (int e = 0; e < 4; e += 2) { const int q = n * 4 + e; const unsigned w = xw[q >> 1];
;                             const f32x2 xv = {__builtin_bit_cast(float, w << 16), __builtin_bit_cast(float, w & 0xffff0000u)}, av = {acc[ai][bj][m][n][e], acc[ai][bj][m][n][e + 1]}, gv = {gp[bj][q], gp[bj][q + 1]};
;                             const f32x2 ov = xv + av * (gv * rF); s2p += ov * ov; o[q] = ov[0]; o[q + 1] = ov[1]; }
;                     if (OUT) { float* op = OUT + (size_t)row * 1024 + col0 + bj * HALF;
;                         __builtin_nontemporal_store((f32x4){o[0], o[1], o[2], o[3]}, (f32x4*)op); __builtin_nontemporal_store((f32x4){o[4], o[5], o[6], o[7]}, (f32x4*)(op + 4)); }
;                     else { u32x4 w; w.x = cvt_pk_bf16(o[0], o[1]); w.y = cvt_pk_bf16(o[2], o[3]); w.z = cvt_pk_bf16(o[4], o[5]); w.w = cvt_pk_bf16(o[6], o[7]);
;                         *(u32x4*)(XB + (size_t)row * 1024 + col0 + bj * HALF) = w; } }
;                 float s2 = s2p[0] + s2p[1];
;                 s2 += epi_xor16(s2); s2 += epi_xor32(s2, lane);
;                 if (fq == 0) scr[wc * 256 + (row & 255)] = s2; }
.LBB0_626:
	v_pk_mul_f32 v[130:131], v[130:131], v[130:131]
	s_nop 0
	v_pk_fma_f32 v[128:129], v[128:129], v[128:129], v[130:131]
	s_nop 0
	v_pk_fma_f32 v[124:125], v[124:125], v[124:125], v[128:129]
	s_nop 0
	v_pk_fma_f32 v[124:125], v[126:127], v[126:127], v[124:125]
	s_nop 0
	v_pk_fma_f32 v[120:121], v[120:121], v[120:121], v[124:125]
	s_nop 0
	v_pk_fma_f32 v[120:121], v[122:123], v[122:123], v[120:121]
	s_nop 0
	v_pk_fma_f32 v[116:117], v[116:117], v[116:117], v[120:121]
	s_nop 0
	v_pk_fma_f32 v[116:117], v[118:119], v[118:119], v[116:117]
	s_nop 0
	v_add_f32_e32 v116, v116, v117
	v_mov_b32_e32 v117, v116
	s_nop 1
	v_permlane16_swap_b32_e32 v117, v116
	s_waitcnt lgkmcnt(0)
	v_add_f32_e32 v116, v116, v117
	v_mov_b32_e32 v117, v116
	s_nop 1
	v_permlane32_swap_b32_e32 v117, v116
	s_and_saveexec_b64 s[0:1], s[2:3]
	s_cbranch_execz .LBB0_628
	s_waitcnt lgkmcnt(0)
	v_add_f32_e32 v116, v116, v117
	v_lshl_add_u32 v117, v138, 2, s51
	ds_write_b32 v117, v116

; __device__ __forceinline__ unsigned cvt_pk_bf16(float lo, float hi) { unsigned r; asm volatile("v_cvt_pk_bf16_f32 %0, %1, %2" : "=v"(r) : "v"(lo), "v"(hi)); return r; }
; __device__ __forceinline__ float epi_xor16(float v) { return __builtin_bit_cast(float, __builtin_amdgcn_ds_swizzle(__builtin_bit_cast(int, v), (16 << 10) | 0x1f)); }
; __device__ __forceinline__ float epi_xor32(float v, int lane) { return __builtin_bit_cast(float, __builtin_amdgcn_ds_bpermute((lane ^ 32) << 2, __builtin_bit_cast(int, v))); }
;     __device__ __forceinline__ void operator()(const f32x4 (&acc)[2][2][4][2], const Unit& u, int wr, int wc, int fr, int fq) const {
;     ...
;                         for (int e = 0; e < 4; e += 2) { const int q = n * 4 + e; const unsigned w = xw[q >> 1];
;                             const f32x2 xv = {__builtin_bit_cast(float, w << 16), __builtin_bit_cast(float, w & 0xffff0000u)}, av = {acc[ai][bj][m][n][e], acc[ai][bj][m][n][e + 1]}, gv = {gp[bj][q], gp[bj][q + 1]};
;                             const f32x2 ov = xv + av * (gv * rF); s2p += ov * ov; o[q] = ov[0]; o[q + 1] = ov[1]; }
;                     if (OUT) { float* op = OUT + (size_t)row * 1024 + col0 + bj * HALF;
;                         __builtin_nontemporal_store((f32x4){o[0], o[1], o[2], o[3]}, (f32x4*)op); __builtin_nontemporal_store((f32x4){o[4], o[5], o[6], o[7]}, (f32x4*)(op + 4)); }
;                     else { u32x4 w; w.x = cvt_pk_bf16(o[0], o[1]); w.y = cvt_pk_bf16(o[2], o[3]); w.z = cvt_pk_bf16(o[4], o[5]); w.w = cvt_pk_bf16(o[6], o[7]);
;                         *(u32x4*)(XB + (size_t)row * 1024 + col0 + bj * HALF) = w; } }
;                 float s2 = s2p[0] + s2p[1];
;                 s2 += epi_xor16(s2); s2 += epi_xor32(s2, lane);
;                 if (fq == 0) scr[wc * 256 + (row & 255)] = s2; }
.LBB0_634:
	v_pk_mul_f32 v[114:115], v[114:115], v[114:115]
	s_nop 0
	v_pk_fma_f32 v[112:113], v[112:113], v[112:113], v[114:115]
	s_nop 0
	v_pk_fma_f32 v[108:109], v[108:109], v[108:109], v[112:113]
	s_nop 0
	v_pk_fma_f32 v[108:109], v[110:111], v[110:111], v[108:109]
	s_nop 0
	v_pk_fma_f32 v[104:105], v[104:105], v[104:105], v[108:109]
	s_nop 0
	v_pk_fma_f32 v[104:105], v[106:107], v[106:107], v[104:105]
	s_nop 0
	v_pk_fma_f32 v[100:101], v[100:101], v[100:101], v[104:105]
	s_nop 0
	v_pk_fma_f32 v[100:101], v[102:103], v[102:103], v[100:101]
	s_nop 0
	v_add_f32_e32 v100, v100, v101
	v_mov_b32_e32 v101, v100
	s_nop 1
	v_permlane16_swap_b32_e32 v101, v100
	s_waitcnt lgkmcnt(0)
	v_add_f32_e32 v100, v100, v101
	v_mov_b32_e32 v101, v100
	s_nop 1
	v_permlane32_swap_b32_e32 v101, v100
	s_and_saveexec_b64 s[0:1], s[2:3]
	s_cbranch_execz .LBB0_636
	s_waitcnt lgkmcnt(0)
	v_add_f32_e32 v100, v100, v101
	v_lshl_add_u32 v101, v122, 2, s51
	ds_write_b32 v101, v100

; __device__ __forceinline__ unsigned cvt_pk_bf16(float lo, float hi) { unsigned r; asm volatile("v_cvt_pk_bf16_f32 %0, %1, %2" : "=v"(r) : "v"(lo), "v"(hi)); return r; }
; __device__ __forceinline__ float epi_xor16(float v) { return __builtin_bit_cast(float, __builtin_amdgcn_ds_swizzle(__builtin_bit_cast(int, v), (16 << 10) | 0x1f)); }
; __device__ __forceinline__ float epi_xor32(float v, int lane) { return __builtin_bit_cast(float, __builtin_amdgcn_ds_bpermute((lane ^ 32) << 2, __builtin_bit_cast(int, v))); }
;     __device__ __forceinline__ void operator()(const f32x4 (&acc)[2][2][4][2], const Unit& u, int wr, int wc, int fr, int fq) const {
;     ...
;                         for (int e = 0; e < 4; e += 2) { const int q = n * 4 + e; const unsigned w = xw[q >> 1];
;                             const f32x2 xv = {__builtin_bit_cast(float, w << 16), __builtin_bit_cast(float, w & 0xffff0000u)}, av = {acc[ai][bj][m][n][e], acc[ai][bj][m][n][e + 1]}, gv = {gp[bj][q], gp[bj][q + 1]};
;                             const f32x2 ov = xv + av * (gv * rF); s2p += ov * ov; o[q] = ov[0]; o[q + 1] = ov[1]; }
;                     if (OUT) { float* op = OUT + (size_t)row * 1024 + col0 + bj * HALF;
;                         __builtin_nontemporal_store((f32x4){o[0], o[1], o[2], o[3]}, (f32x4*)op); __builtin_nontemporal_store((f32x4){o[4], o[5], o[6], o[7]}, (f32x4*)(op + 4)); }
;                     else { u32x4 w; w.x = cvt_pk_bf16(o[0], o[1]); w.y = cvt_pk_bf16(o[2], o[3]); w.z = cvt_pk_bf16(o[4], o[5]); w.w = cvt_pk_bf16(o[6], o[7]);
;                         *(u32x4*)(XB + (size_t)row * 1024 + col0 + bj * HALF) = w; } }
;                 float s2 = s2p[0] + s2p[1];
;                 s2 += epi_xor16(s2); s2 += epi_xor32(s2, lane);
;                 if (fq == 0) scr[wc * 256 + (row & 255)] = s2; }
.LBB0_642:
	v_pk_mul_f32 v[98:99], v[98:99], v[98:99]
	s_nop 0
	v_pk_fma_f32 v[96:97], v[96:97], v[96:97], v[98:99]
	s_nop 0
	v_pk_fma_f32 v[92:93], v[92:93], v[92:93], v[96:97]
	s_nop 0
	v_pk_fma_f32 v[92:93], v[94:95], v[94:95], v[92:93]
	s_nop 0
	v_pk_fma_f32 v[88:89], v[88:89], v[88:89], v[92:93]
	s_nop 0
	v_pk_fma_f32 v[88:89], v[90:91], v[90:91], v[88:89]
	s_nop 0
	v_pk_fma_f32 v[84:85], v[84:85], v[84:85], v[88:89]
	s_nop 0
	v_pk_fma_f32 v[84:85], v[86:87], v[86:87], v[84:85]
	s_nop 0
	v_add_f32_e32 v84, v84, v85
	v_mov_b32_e32 v85, v84
	s_nop 1
	v_permlane16_swap_b32_e32 v85, v84
	s_waitcnt lgkmcnt(0)
	v_add_f32_e32 v84, v84, v85
	v_mov_b32_e32 v85, v84
	s_nop 1
	v_permlane32_swap_b32_e32 v85, v84
	s_and_saveexec_b64 s[0:1], s[2:3]
	s_cbranch_execz .LBB0_644
	v_lshl_add_u32 v86, v106, 2, s51
	s_waitcnt lgkmcnt(0)
	v_add_f32_e32 v84, v84, v85
	ds_write_b32 v86, v84

; __device__ __forceinline__ unsigned cvt_pk_bf16(float lo, float hi) { unsigned r; asm volatile("v_cvt_pk_bf16_f32 %0, %1, %2" : "=v"(r) : "v"(lo), "v"(hi)); return r; }
; __device__ __forceinline__ float epi_xor16(float v) { return __builtin_bit_cast(float, __builtin_amdgcn_ds_swizzle(__builtin_bit_cast(int, v), (16 << 10) | 0x1f)); }
; __device__ __forceinline__ float epi_xor32(float v, int lane) { return __builtin_bit_cast(float, __builtin_amdgcn_ds_bpermute((lane ^ 32) << 2, __builtin_bit_cast(int, v))); }
;     __device__ __forceinline__ void operator()(const f32x4 (&acc)[2][2][4][2], const Unit& u, int wr, int wc, int fr, int fq) const {
;     ...
;                         for (int e = 0; e < 4; e += 2) { const int q = n * 4 + e; const unsigned w = xw[q >> 1];
;                             const f32x2 xv = {__builtin_bit_cast(float, w << 16), __builtin_bit_cast(float, w & 0xffff0000u)}, av = {acc[ai][bj][m][n][e], acc[ai][bj][m][n][e + 1]}, gv = {gp[bj][q], gp[bj][q + 1]};
;                             const f32x2 ov = xv + av * (gv * rF); s2p += ov * ov; o[q] = ov[0]; o[q + 1] = ov[1]; }
;                     if (OUT) { float* op = OUT + (size_t)row * 1024 + col0 + bj * HALF;
;                         __builtin_nontemporal_store((f32x4){o[0], o[1], o[2], o[3]}, (f32x4*)op); __builtin_nontemporal_store((f32x4){o[4], o[5], o[6], o[7]}, (f32x4*)(op + 4)); }
;                     else { u32x4 w; w.x = cvt_pk_bf16(o[0], o[1]); w.y = cvt_pk_bf16(o[2], o[3]); w.z = cvt_pk_bf16(o[4], o[5]); w.w = cvt_pk_bf16(o[6], o[7]);
;                         *(u32x4*)(XB + (size_t)row * 1024 + col0 + bj * HALF) = w; } }
;                 float s2 = s2p[0] + s2p[1];
;                 s2 += epi_xor16(s2); s2 += epi_xor32(s2, lane);
;                 if (fq == 0) scr[wc * 256 + (row & 255)] = s2; }
.LBB0_650:
	v_pk_mul_f32 v[74:75], v[74:75], v[74:75]
	s_nop 0
	v_pk_fma_f32 v[72:73], v[72:73], v[72:73], v[74:75]
	s_nop 0
	v_pk_fma_f32 v[64:65], v[64:65], v[64:65], v[72:73]
	s_nop 0
	v_pk_fma_f32 v[64:65], v[66:67], v[66:67], v[64:65]
	s_nop 0
	v_pk_fma_f32 v[56:57], v[56:57], v[56:57], v[64:65]
	s_nop 0
	v_pk_fma_f32 v[56:57], v[58:59], v[58:59], v[56:57]
	s_nop 0
	v_pk_fma_f32 v[52:53], v[52:53], v[52:53], v[56:57]
	s_nop 0
	v_pk_fma_f32 v[52:53], v[54:55], v[54:55], v[52:53]
	s_nop 0
	v_add_f32_e32 v52, v52, v53
	v_mov_b32_e32 v53, v52
	s_nop 1
	v_permlane16_swap_b32_e32 v53, v52
	s_waitcnt lgkmcnt(0)
	v_add_f32_e32 v52, v52, v53
	v_mov_b32_e32 v53, v52
	s_nop 1
	v_permlane32_swap_b32_e32 v53, v52
	s_and_saveexec_b64 s[0:1], s[2:3]
	s_cbranch_execz .LBB0_652
	s_waitcnt lgkmcnt(0)
	v_add_f32_e32 v52, v52, v53
	v_lshl_add_u32 v53, v130, 2, s51
	ds_write_b32 v53, v52

; __device__ __forceinline__ unsigned cvt_pk_bf16(float lo, float hi) { unsigned r; asm volatile("v_cvt_pk_bf16_f32 %0, %1, %2" : "=v"(r) : "v"(lo), "v"(hi)); return r; }
; __device__ __forceinline__ float epi_xor16(float v) { return __builtin_bit_cast(float, __builtin_amdgcn_ds_swizzle(__builtin_bit_cast(int, v), (16 << 10) | 0x1f)); }
; __device__ __forceinline__ float epi_xor32(float v, int lane) { return __builtin_bit_cast(float, __builtin_amdgcn_ds_bpermute((lane ^ 32) << 2, __builtin_bit_cast(int, v))); }
;     __device__ __forceinline__ void operator()(const f32x4 (&acc)[2][2][4][2], const Unit& u, int wr, int wc, int fr, int fq) const {
;     ...
;                         for (int e = 0; e < 4; e += 2) { const int q = n * 4 + e; const unsigned w = xw[q >> 1];
;                             const f32x2 xv = {__builtin_bit_cast(float, w << 16), __builtin_bit_cast(float, w & 0xffff0000u)}, av = {acc[ai][bj][m][n][e], acc[ai][bj][m][n][e + 1]}, gv = {gp[bj][q], gp[bj][q + 1]};
;                             const f32x2 ov = xv + av * (gv * rF); s2p += ov * ov; o[q] = ov[0]; o[q + 1] = ov[1]; }
;                     if (OUT) { float* op = OUT + (size_t)row * 1024 + col0 + bj * HALF;
;                         __builtin_nontemporal_store((f32x4){o[0], o[1], o[2], o[3]}, (f32x4*)op); __builtin_nontemporal_store((f32x4){o[4], o[5], o[6], o[7]}, (f32x4*)(op + 4)); }
;                     else { u32x4 w; w.x = cvt_pk_bf16(o[0], o[1]); w.y = cvt_pk_bf16(o[2], o[3]); w.z = cvt_pk_bf16(o[4], o[5]); w.w = cvt_pk_bf16(o[6], o[7]);
;                         *(u32x4*)(XB + (size_t)row * 1024 + col0 + bj * HALF) = w; } }
;                 float s2 = s2p[0] + s2p[1];
;                 s2 += epi_xor16(s2); s2 += epi_xor32(s2, lane);
;                 if (fq == 0) scr[wc * 256 + (row & 255)] = s2; }
.LBB0_658:
	v_pk_mul_f32 v[50:51], v[50:51], v[50:51]
	s_nop 0
	v_pk_fma_f32 v[48:49], v[48:49], v[48:49], v[50:51]
	s_nop 0
	v_pk_fma_f32 v[44:45], v[44:45], v[44:45], v[48:49]
	s_nop 0
	v_pk_fma_f32 v[44:45], v[46:47], v[46:47], v[44:45]
	s_nop 0
	v_pk_fma_f32 v[40:41], v[40:41], v[40:41], v[44:45]
	s_nop 0
	v_pk_fma_f32 v[40:41], v[42:43], v[42:43], v[40:41]
	s_nop 0
	v_pk_fma_f32 v[36:37], v[36:37], v[36:37], v[40:41]
	s_nop 0
	v_pk_fma_f32 v[36:37], v[38:39], v[38:39], v[36:37]
	s_nop 0
	v_add_f32_e32 v36, v36, v37
	v_mov_b32_e32 v37, v36
	s_nop 1
	v_permlane16_swap_b32_e32 v37, v36
	s_waitcnt lgkmcnt(0)
	v_add_f32_e32 v36, v36, v37
	v_mov_b32_e32 v37, v36
	s_nop 1
	v_permlane32_swap_b32_e32 v37, v36
	s_and_saveexec_b64 s[0:1], s[2:3]
	s_cbranch_execz .LBB0_660
	s_waitcnt lgkmcnt(0)
	v_add_f32_e32 v36, v36, v37
	v_lshl_add_u32 v37, v58, 2, s51
	ds_write_b32 v37, v36

; __device__ __forceinline__ unsigned cvt_pk_bf16(float lo, float hi) { unsigned r; asm volatile("v_cvt_pk_bf16_f32 %0, %1, %2" : "=v"(r) : "v"(lo), "v"(hi)); return r; }
; __device__ __forceinline__ float epi_xor16(float v) { return __builtin_bit_cast(float, __builtin_amdgcn_ds_swizzle(__builtin_bit_cast(int, v), (16 << 10) | 0x1f)); }
; __device__ __forceinline__ float epi_xor32(float v, int lane) { return __builtin_bit_cast(float, __builtin_amdgcn_ds_bpermute((lane ^ 32) << 2, __builtin_bit_cast(int, v))); }
;     __device__ __forceinline__ void operator()(const f32x4 (&acc)[2][2][4][2], const Unit& u, int wr, int wc, int fr, int fq) const {
;     ...
;                         for (int e = 0; e < 4; e += 2) { const int q = n * 4 + e; const unsigned w = xw[q >> 1];
;                             const f32x2 xv = {__builtin_bit_cast(float, w << 16), __builtin_bit_cast(float, w & 0xffff0000u)}, av = {acc[ai][bj][m][n][e], acc[ai][bj][m][n][e + 1]}, gv = {gp[bj][q], gp[bj][q + 1]};
;                             const f32x2 ov = xv + av * (gv * rF); s2p += ov * ov; o[q] = ov[0]; o[q + 1] = ov[1]; }
;                     if (OUT) { float* op = OUT + (size_t)row * 1024 + col0 + bj * HALF;
;                         __builtin_nontemporal_store((f32x4){o[0], o[1], o[2], o[3]}, (f32x4*)op); __builtin_nontemporal_store((f32x4){o[4], o[5], o[6], o[7]}, (f32x4*)(op + 4)); }
;                     else { u32x4 w; w.x = cvt_pk_bf16(o[0], o[1]); w.y = cvt_pk_bf16(o[2], o[3]); w.z = cvt_pk_bf16(o[4], o[5]); w.w = cvt_pk_bf16(o[6], o[7]);
;                         *(u32x4*)(XB + (size_t)row * 1024 + col0 + bj * HALF) = w; } }
;                 float s2 = s2p[0] + s2p[1];
;                 s2 += epi_xor16(s2); s2 += epi_xor32(s2, lane);
;                 if (fq == 0) scr[wc * 256 + (row & 255)] = s2; }
.LBB0_666:
	v_pk_mul_f32 v[34:35], v[34:35], v[34:35]
	s_nop 0
	v_pk_fma_f32 v[32:33], v[32:33], v[32:33], v[34:35]
	s_nop 0
	v_pk_fma_f32 v[28:29], v[28:29], v[28:29], v[32:33]
	s_nop 0
	v_pk_fma_f32 v[28:29], v[30:31], v[30:31], v[28:29]
	s_nop 0
	v_pk_fma_f32 v[24:25], v[24:25], v[24:25], v[28:29]
	s_nop 0
	v_pk_fma_f32 v[24:25], v[26:27], v[26:27], v[24:25]
	s_nop 0
	v_pk_fma_f32 v[20:21], v[20:21], v[20:21], v[24:25]
	s_nop 0
	v_pk_fma_f32 v[20:21], v[22:23], v[22:23], v[20:21]
	s_nop 0
	v_add_f32_e32 v20, v20, v21
	v_mov_b32_e32 v21, v20
	s_nop 1
	v_permlane16_swap_b32_e32 v21, v20
	s_waitcnt lgkmcnt(0)
	v_add_f32_e32 v20, v20, v21
	v_mov_b32_e32 v21, v20
	s_nop 1
	v_permlane32_swap_b32_e32 v21, v20
	s_and_saveexec_b64 s[0:1], s[2:3]
	s_cbranch_execz .LBB0_668
	s_waitcnt lgkmcnt(0)
	v_add_f32_e32 v20, v20, v21
	v_lshl_add_u32 v21, v42, 2, s51
	ds_write_b32 v21, v20

; __device__ __forceinline__ unsigned cvt_pk_bf16(float lo, float hi) { unsigned r; asm volatile("v_cvt_pk_bf16_f32 %0, %1, %2" : "=v"(r) : "v"(lo), "v"(hi)); return r; }
; __device__ __forceinline__ float epi_xor16(float v) { return __builtin_bit_cast(float, __builtin_amdgcn_ds_swizzle(__builtin_bit_cast(int, v), (16 << 10) | 0x1f)); }
; __device__ __forceinline__ float epi_xor32(float v, int lane) { return __builtin_bit_cast(float, __builtin_amdgcn_ds_bpermute((lane ^ 32) << 2, __builtin_bit_cast(int, v))); }
;     __device__ __forceinline__ void operator()(const f32x4 (&acc)[2][2][4][2], const Unit& u, int wr, int wc, int fr, int fq) const {
;     ...
;                         for (int e = 0; e < 4; e += 2) { const int q = n * 4 + e; const unsigned w = xw[q >> 1];
;                             const f32x2 xv = {__builtin_bit_cast(float, w << 16), __builtin_bit_cast(float, w & 0xffff0000u)}, av = {acc[ai][bj][m][n][e], acc[ai][bj][m][n][e + 1]}, gv = {gp[bj][q], gp[bj][q + 1]};
;                             const f32x2 ov = xv + av * (gv * rF); s2p += ov * ov; o[q] = ov[0]; o[q + 1] = ov[1]; }
;                     if (OUT) { float* op = OUT + (size_t)row * 1024 + col0 + bj * HALF;
;                         __builtin_nontemporal_store((f32x4){o[0], o[1], o[2], o[3]}, (f32x4*)op); __builtin_nontemporal_store((f32x4){o[4], o[5], o[6], o[7]}, (f32x4*)(op + 4)); }
;                     else { u32x4 w; w.x = cvt_pk_bf16(o[0], o[1]); w.y = cvt_pk_bf16(o[2], o[3]); w.z = cvt_pk_bf16(o[4], o[5]); w.w = cvt_pk_bf16(o[6], o[7]);
;                         *(u32x4*)(XB + (size_t)row * 1024 + col0 + bj * HALF) = w; } }
;                 float s2 = s2p[0] + s2p[1];
;                 s2 += epi_xor16(s2); s2 += epi_xor32(s2, lane);
;                 if (fq == 0) scr[wc * 256 + (row & 255)] = s2; }
.LBB0_674:
	v_pk_mul_f32 v[18:19], v[18:19], v[18:19]
	s_nop 0
	v_pk_fma_f32 v[16:17], v[16:17], v[16:17], v[18:19]
	s_nop 0
	v_pk_fma_f32 v[12:13], v[12:13], v[12:13], v[16:17]
	s_nop 0
	v_pk_fma_f32 v[12:13], v[14:15], v[14:15], v[12:13]
	s_nop 0
	v_pk_fma_f32 v[8:9], v[8:9], v[8:9], v[12:13]
	s_nop 0
	v_pk_fma_f32 v[8:9], v[10:11], v[10:11], v[8:9]
	s_nop 0
	v_pk_fma_f32 v[4:5], v[4:5], v[4:5], v[8:9]
	s_nop 0
	v_pk_fma_f32 v[4:5], v[6:7], v[6:7], v[4:5]
	s_nop 0
	v_add_f32_e32 v4, v4, v5
	v_mov_b32_e32 v5, v4
	s_nop 1
	v_permlane16_swap_b32_e32 v5, v4
	s_waitcnt lgkmcnt(0)
	v_add_f32_e32 v4, v4, v5
	v_mov_b32_e32 v5, v4
	s_nop 1
	v_permlane32_swap_b32_e32 v5, v4
	s_and_saveexec_b64 s[0:1], s[2:3]
	s_cbranch_execz .LBB0_676
	v_lshl_add_u32 v6, v26, 2, s51
	s_waitcnt lgkmcnt(0)
	v_add_f32_e32 v4, v4, v5
	ds_write_b32 v6, v4
